# back-edge rotation (sec 7.11): K-loop head SALU block and counter increments hoisted into the MFMA shadow of the last MMA segment in up/down/in-proj/out GEMM loops and their peels
# speedup vs baseline: 1.0144x; 1.0144x over previous
.LBB0_390:
	s_add_u32 s1, s42, 0x100
	v_lshl_add_u64 v[142:143], s[40:41], 0, v[130:131]
	s_addc_u32 s24, s43, 0
	s_mov_b32 s25, -2
	s_mov_b64 s[42:43], 0
	s_add_u32 s14, s40, s42
	s_addc_u32 s15, s41, s43
	s_add_u32 s34, s14, 0x100
	s_addc_u32 s35, s15, 0
	s_add_u32 s44, s1, s42
	s_addc_u32 s45, s24, s43
	s_cmpk_eq_i32 s42, 0x700
	s_cselect_b64 vcc, -1, 0
	s_and_b64 s[14:15], vcc, exec
	s_cselect_b32 s15, s55, s35
	s_cselect_b32 s14, s54, s34
	s_cselect_b32 s35, s69, s45
	s_cselect_b32 s34, s68, s44
	s_add_i32 s44, 0, 0x11000
	v_add_u32_e32 v145, s44, v1
	s_add_i32 s45, 0, 0x15000
	ds_read_b128 v[146:149], v145
	ds_read_b128 v[150:153], v145 offset:1024
	ds_read_b128 v[154:157], v145 offset:2048
	ds_read_b128 v[158:161], v145 offset:3072
	v_add_u32_e32 v145, s45, v1
	ds_read_b128 v[162:165], v145
	ds_read_b128 v[166:169], v145 offset:1024
	ds_read_b128 v[170:173], v145 offset:2048
	ds_read_b128 v[174:177], v145 offset:3072
	v_cndmask_b32_e32 v193, v131, v141, vcc
	v_cndmask_b32_e32 v192, v130, v140, vcc
	v_lshl_add_u64 v[220:221], v[142:143], 0, s[42:43]
	v_lshl_add_u64 v[222:223], v[220:221], 0, s[6:7]
	s_add_i32 m0, s28, 0xd000
	ds_read_b128 v[178:181], v144 offset:4096
	ds_read_b128 v[182:185], v144 offset:5120
	ds_read_b128 v[196:199], v144 offset:6144
	ds_read_b128 v[200:203], v144 offset:7168
	ds_read_b128 v[204:207], v144 offset:8192
	ds_read_b128 v[208:211], v144 offset:9216
	ds_read_b128 v[212:215], v144 offset:10240
	ds_read_b128 v[216:219], v144 offset:11264
	global_load_lds_dwordx4 v[222:223], off
	v_lshl_add_u64 v[220:221], v[220:221], 0, s[8:9]
	s_add_i32 m0, s28, 0xf000
	s_nop 0
	global_load_lds_dwordx4 v[220:221], off
	s_waitcnt vmcnt(8)
	s_waitcnt lgkmcnt(0)
	s_barrier
	s_setprio 1
	s_waitcnt lgkmcnt(0)
	v_mfma_f32_16x16x32_bf16 v[126:129], v[146:149], v[178:181], 0
	v_mfma_f32_16x16x32_bf16 v[122:125], v[154:157], v[178:181], 0
	v_mfma_f32_16x16x32_bf16 v[110:113], v[146:149], v[196:199], 0
	v_mfma_f32_16x16x32_bf16 v[106:109], v[154:157], v[196:199], 0
	v_mfma_f32_16x16x32_bf16 v[94:97], v[146:149], v[204:207], 0
	v_mfma_f32_16x16x32_bf16 v[90:93], v[154:157], v[204:207], 0
	v_mfma_f32_16x16x32_bf16 v[78:81], v[146:149], v[212:215], 0
	v_mfma_f32_16x16x32_bf16 v[74:77], v[154:157], v[212:215], 0
	v_mfma_f32_16x16x32_bf16 v[126:129], v[150:153], v[182:185], v[126:129]
	v_mfma_f32_16x16x32_bf16 v[122:125], v[158:161], v[182:185], v[122:125]
	v_mfma_f32_16x16x32_bf16 v[110:113], v[150:153], v[200:203], v[110:113]
	v_mfma_f32_16x16x32_bf16 v[106:109], v[158:161], v[200:203], v[106:109]
	v_mfma_f32_16x16x32_bf16 v[94:97], v[150:153], v[208:211], v[94:97]
	v_mfma_f32_16x16x32_bf16 v[90:93], v[158:161], v[208:211], v[90:93]
	v_mfma_f32_16x16x32_bf16 v[78:81], v[150:153], v[216:219], v[78:81]
	v_mfma_f32_16x16x32_bf16 v[74:77], v[158:161], v[216:219], v[74:77]
	s_setprio 0
	s_setprio 1
	v_mfma_f32_16x16x32_bf16 v[118:121], v[162:165], v[178:181], 0
	v_mfma_f32_16x16x32_bf16 v[114:117], v[170:173], v[178:181], 0
	v_mfma_f32_16x16x32_bf16 v[102:105], v[162:165], v[196:199], 0
	v_mfma_f32_16x16x32_bf16 v[98:101], v[170:173], v[196:199], 0
	v_mfma_f32_16x16x32_bf16 v[86:89], v[162:165], v[204:207], 0
	v_mfma_f32_16x16x32_bf16 v[82:85], v[170:173], v[204:207], 0
	v_mfma_f32_16x16x32_bf16 v[70:73], v[162:165], v[212:215], 0
	v_mfma_f32_16x16x32_bf16 v[66:69], v[170:173], v[212:215], 0
	v_mfma_f32_16x16x32_bf16 v[118:121], v[166:169], v[182:185], v[118:121]
	v_mfma_f32_16x16x32_bf16 v[114:117], v[174:177], v[182:185], v[114:117]
	v_mfma_f32_16x16x32_bf16 v[102:105], v[166:169], v[200:203], v[102:105]
	v_mfma_f32_16x16x32_bf16 v[98:101], v[174:177], v[200:203], v[98:101]
	v_mfma_f32_16x16x32_bf16 v[86:89], v[166:169], v[208:211], v[86:89]
	v_mfma_f32_16x16x32_bf16 v[82:85], v[174:177], v[208:211], v[82:85]
	v_mfma_f32_16x16x32_bf16 v[70:73], v[166:169], v[216:219], v[70:73]
	v_mfma_f32_16x16x32_bf16 v[66:69], v[174:177], v[216:219], v[66:69]
	s_setprio 0
	s_barrier
	s_add_i32 s44, s44, s12
	v_lshl_add_u64 v[220:221], s[34:35], 0, v[186:187]
	s_mov_b32 m0, s44
	ds_read_b128 v[178:181], v144 offset:20480
	ds_read_b128 v[182:185], v144 offset:21504
	ds_read_b128 v[196:199], v144 offset:22528
	ds_read_b128 v[200:203], v144 offset:23552
	ds_read_b128 v[204:207], v144 offset:24576
	ds_read_b128 v[208:211], v144 offset:25600
	ds_read_b128 v[212:215], v144 offset:26624
	ds_read_b128 v[216:219], v144 offset:27648
	global_load_lds_dwordx4 v186, s[34:35]
	v_lshl_add_u64 v[222:223], v[220:221], 0, s[82:83]
	s_add_i32 m0, s44, 0x2000
	s_add_i32 s34, s45, s12
	global_load_lds_dwordx4 v[222:223], off
	v_lshl_add_u64 v[222:223], v[220:221], 0, s[64:65]
	s_mov_b32 m0, s34
	v_lshl_add_u64 v[192:193], s[14:15], 0, v[192:193]
	global_load_lds_dwordx4 v[222:223], off
	v_lshl_add_u64 v[222:223], v[220:221], 0, s[86:87]
	s_add_i32 m0, s34, 0x2000
	s_nop 0
	global_load_lds_dwordx4 v[222:223], off
	s_mov_b32 m0, s29
	v_lshl_add_u64 v[222:223], v[192:193], 0, s[82:83]
	global_load_lds_dwordx4 v[192:193], off
	s_mov_b32 m0, s47
	s_nop 0
	global_load_lds_dwordx4 v[222:223], off
	s_waitcnt vmcnt(8)
	s_waitcnt lgkmcnt(0)
	s_barrier
	s_setprio 1
	s_waitcnt lgkmcnt(0)
	v_mfma_f32_16x16x32_bf16 v[62:65], v[146:149], v[178:181], 0
	v_mfma_f32_16x16x32_bf16 v[58:61], v[154:157], v[178:181], 0
	v_mfma_f32_16x16x32_bf16 v[46:49], v[146:149], v[196:199], 0
	v_mfma_f32_16x16x32_bf16 v[42:45], v[154:157], v[196:199], 0
	v_mfma_f32_16x16x32_bf16 v[30:33], v[146:149], v[204:207], 0
	v_mfma_f32_16x16x32_bf16 v[26:29], v[154:157], v[204:207], 0
	v_mfma_f32_16x16x32_bf16 v[14:17], v[146:149], v[212:215], 0
	v_mfma_f32_16x16x32_bf16 v[10:13], v[154:157], v[212:215], 0
	v_mfma_f32_16x16x32_bf16 v[62:65], v[150:153], v[182:185], v[62:65]
	v_mfma_f32_16x16x32_bf16 v[58:61], v[158:161], v[182:185], v[58:61]
	v_mfma_f32_16x16x32_bf16 v[46:49], v[150:153], v[200:203], v[46:49]
	v_mfma_f32_16x16x32_bf16 v[42:45], v[158:161], v[200:203], v[42:45]
	v_mfma_f32_16x16x32_bf16 v[30:33], v[150:153], v[208:211], v[30:33]
	v_mfma_f32_16x16x32_bf16 v[26:29], v[158:161], v[208:211], v[26:29]
	v_mfma_f32_16x16x32_bf16 v[14:17], v[150:153], v[216:219], v[14:17]
	v_mfma_f32_16x16x32_bf16 v[10:13], v[158:161], v[216:219], v[10:13]
	s_setprio 0
	s_setprio 1
	v_mfma_f32_16x16x32_bf16 v[54:57], v[162:165], v[178:181], 0
	v_mfma_f32_16x16x32_bf16 v[50:53], v[170:173], v[178:181], 0
	v_mfma_f32_16x16x32_bf16 v[38:41], v[162:165], v[196:199], 0
	v_mfma_f32_16x16x32_bf16 v[34:37], v[170:173], v[196:199], 0
	v_mfma_f32_16x16x32_bf16 v[22:25], v[162:165], v[204:207], 0
	v_mfma_f32_16x16x32_bf16 v[18:21], v[170:173], v[204:207], 0
	v_mfma_f32_16x16x32_bf16 v[6:9], v[162:165], v[212:215], 0
	v_mfma_f32_16x16x32_bf16 v[2:5], v[170:173], v[212:215], 0
	v_mfma_f32_16x16x32_bf16 v[54:57], v[166:169], v[182:185], v[54:57]
	v_mfma_f32_16x16x32_bf16 v[50:53], v[174:177], v[182:185], v[50:53]
	v_mfma_f32_16x16x32_bf16 v[38:41], v[166:169], v[200:203], v[38:41]
	v_mfma_f32_16x16x32_bf16 v[34:37], v[174:177], v[200:203], v[34:37]
	v_mfma_f32_16x16x32_bf16 v[22:25], v[166:169], v[208:211], v[22:25]
	v_mfma_f32_16x16x32_bf16 v[18:21], v[174:177], v[208:211], v[18:21]
	v_mfma_f32_16x16x32_bf16 v[6:9], v[166:169], v[216:219], v[6:9]
	v_mfma_f32_16x16x32_bf16 v[2:5], v[174:177], v[216:219], v[2:5]
	s_setprio 0
	s_barrier
	s_add_i32 s14, 0, 0x19000
	v_add_u32_e32 v145, s14, v1
	s_add_i32 s15, 0, 0x1d000
	ds_read_b128 v[146:149], v145
	ds_read_b128 v[150:153], v145 offset:1024
	ds_read_b128 v[154:157], v145 offset:2048
	ds_read_b128 v[158:161], v145 offset:3072
	v_add_u32_e32 v145, s15, v1
	ds_read_b128 v[162:165], v145
	ds_read_b128 v[166:169], v145 offset:1024
	ds_read_b128 v[170:173], v145 offset:2048
	ds_read_b128 v[174:177], v145 offset:3072
	s_mov_b32 m0, s60
	v_lshl_add_u64 v[222:223], v[192:193], 0, s[64:65]
	ds_read_b128 v[178:181], v144 offset:36864
	ds_read_b128 v[182:185], v144 offset:37888
	ds_read_b128 v[196:199], v144 offset:38912
	ds_read_b128 v[200:203], v144 offset:39936
	ds_read_b128 v[204:207], v144 offset:40960
	ds_read_b128 v[208:211], v144 offset:41984
	ds_read_b128 v[212:215], v144 offset:43008
	ds_read_b128 v[216:219], v144 offset:44032
	global_load_lds_dwordx4 v[222:223], off
	v_lshl_add_u64 v[222:223], v[192:193], 0, s[86:87]
	s_mov_b32 m0, s61
	s_nop 0
	global_load_lds_dwordx4 v[222:223], off
	s_waitcnt vmcnt(8)
	s_waitcnt lgkmcnt(0)
	s_barrier
	s_setprio 1
	s_waitcnt lgkmcnt(0)
	v_mfma_f32_16x16x32_bf16 v[126:129], v[146:149], v[178:181], v[126:129]
	v_mfma_f32_16x16x32_bf16 v[122:125], v[154:157], v[178:181], v[122:125]
	v_mfma_f32_16x16x32_bf16 v[110:113], v[146:149], v[196:199], v[110:113]
	v_mfma_f32_16x16x32_bf16 v[106:109], v[154:157], v[196:199], v[106:109]
	v_mfma_f32_16x16x32_bf16 v[94:97], v[146:149], v[204:207], v[94:97]
	v_mfma_f32_16x16x32_bf16 v[90:93], v[154:157], v[204:207], v[90:93]
	v_mfma_f32_16x16x32_bf16 v[78:81], v[146:149], v[212:215], v[78:81]
	v_mfma_f32_16x16x32_bf16 v[74:77], v[154:157], v[212:215], v[74:77]
	v_mfma_f32_16x16x32_bf16 v[126:129], v[150:153], v[182:185], v[126:129]
	v_mfma_f32_16x16x32_bf16 v[122:125], v[158:161], v[182:185], v[122:125]
	v_mfma_f32_16x16x32_bf16 v[110:113], v[150:153], v[200:203], v[110:113]
	v_mfma_f32_16x16x32_bf16 v[106:109], v[158:161], v[200:203], v[106:109]
	v_mfma_f32_16x16x32_bf16 v[94:97], v[150:153], v[208:211], v[94:97]
	v_mfma_f32_16x16x32_bf16 v[90:93], v[158:161], v[208:211], v[90:93]
	v_mfma_f32_16x16x32_bf16 v[78:81], v[150:153], v[216:219], v[78:81]
	v_mfma_f32_16x16x32_bf16 v[74:77], v[158:161], v[216:219], v[74:77]
	s_setprio 0
	s_setprio 1
	v_mfma_f32_16x16x32_bf16 v[118:121], v[162:165], v[178:181], v[118:121]
	v_mfma_f32_16x16x32_bf16 v[114:117], v[170:173], v[178:181], v[114:117]
	v_mfma_f32_16x16x32_bf16 v[102:105], v[162:165], v[196:199], v[102:105]
	v_mfma_f32_16x16x32_bf16 v[98:101], v[170:173], v[196:199], v[98:101]
	v_mfma_f32_16x16x32_bf16 v[86:89], v[162:165], v[204:207], v[86:89]
	v_mfma_f32_16x16x32_bf16 v[82:85], v[170:173], v[204:207], v[82:85]
	v_mfma_f32_16x16x32_bf16 v[70:73], v[162:165], v[212:215], v[70:73]
	v_mfma_f32_16x16x32_bf16 v[66:69], v[170:173], v[212:215], v[66:69]
	v_mfma_f32_16x16x32_bf16 v[118:121], v[166:169], v[182:185], v[118:121]
	v_mfma_f32_16x16x32_bf16 v[114:117], v[174:177], v[182:185], v[114:117]
	v_mfma_f32_16x16x32_bf16 v[102:105], v[166:169], v[200:203], v[102:105]
	v_mfma_f32_16x16x32_bf16 v[98:101], v[174:177], v[200:203], v[98:101]
	v_mfma_f32_16x16x32_bf16 v[86:89], v[166:169], v[208:211], v[86:89]
	v_mfma_f32_16x16x32_bf16 v[82:85], v[174:177], v[208:211], v[82:85]
	v_mfma_f32_16x16x32_bf16 v[70:73], v[166:169], v[216:219], v[70:73]
	v_mfma_f32_16x16x32_bf16 v[66:69], v[174:177], v[216:219], v[66:69]
	s_setprio 0
	s_barrier
	s_add_i32 s14, s14, s12
	v_lshl_add_u64 v[222:223], v[220:221], 0, s[92:93]
	s_mov_b32 m0, s14
	ds_read_b128 v[178:181], v144 offset:53248
	ds_read_b128 v[182:185], v144 offset:54272
	ds_read_b128 v[196:199], v144 offset:55296
	ds_read_b128 v[200:203], v144 offset:56320
	ds_read_b128 v[204:207], v144 offset:57344
	ds_read_b128 v[208:211], v144 offset:58368
	ds_read_b128 v[212:215], v144 offset:59392
	ds_read_b128 v[216:219], v144 offset:60416
	global_load_lds_dwordx4 v[222:223], off
	v_lshl_add_u64 v[222:223], v[220:221], 0, s[4:5]
	s_add_i32 m0, s14, 0x2000
	s_add_i32 s14, s15, s12
	global_load_lds_dwordx4 v[222:223], off
	v_lshl_add_u64 v[222:223], v[220:221], 0, s[6:7]
	s_mov_b32 m0, s14
	v_lshl_add_u64 v[220:221], v[220:221], 0, s[8:9]
	global_load_lds_dwordx4 v[222:223], off
	s_add_i32 m0, s14, 0x2000
	s_nop 0
	global_load_lds_dwordx4 v[220:221], off
	v_lshl_add_u64 v[220:221], v[192:193], 0, s[92:93]
	s_mov_b32 m0, s76
	v_lshl_add_u64 v[192:193], v[192:193], 0, s[4:5]
	global_load_lds_dwordx4 v[220:221], off
	s_mov_b32 m0, s77
	s_nop 0
	global_load_lds_dwordx4 v[192:193], off
	s_waitcnt vmcnt(8)
	s_waitcnt lgkmcnt(0)
	s_barrier
	s_setprio 1
	s_waitcnt lgkmcnt(0)
	v_mfma_f32_16x16x32_bf16 v[62:65], v[146:149], v[178:181], v[62:65]
	v_mfma_f32_16x16x32_bf16 v[58:61], v[154:157], v[178:181], v[58:61]
	s_add_i32 s25, s25, 2
	v_mfma_f32_16x16x32_bf16 v[46:49], v[146:149], v[196:199], v[46:49]
	s_add_u32 s42, s42, 0x100
	v_mfma_f32_16x16x32_bf16 v[42:45], v[154:157], v[196:199], v[42:45]
	s_addc_u32 s43, s43, 0
	v_mfma_f32_16x16x32_bf16 v[30:33], v[146:149], v[204:207], v[30:33]
	s_add_u32 s14, s40, s42
	v_mfma_f32_16x16x32_bf16 v[26:29], v[154:157], v[204:207], v[26:29]
	s_addc_u32 s15, s41, s43
	v_mfma_f32_16x16x32_bf16 v[14:17], v[146:149], v[212:215], v[14:17]
	s_add_u32 s34, s14, 0x100
	v_mfma_f32_16x16x32_bf16 v[10:13], v[154:157], v[212:215], v[10:13]
	s_addc_u32 s35, s15, 0
	v_mfma_f32_16x16x32_bf16 v[62:65], v[150:153], v[182:185], v[62:65]
	s_add_u32 s44, s1, s42
	v_mfma_f32_16x16x32_bf16 v[58:61], v[158:161], v[182:185], v[58:61]
	s_addc_u32 s45, s24, s43
	v_mfma_f32_16x16x32_bf16 v[46:49], v[150:153], v[200:203], v[46:49]
	s_cmpk_eq_i32 s42, 0x700
	v_mfma_f32_16x16x32_bf16 v[42:45], v[158:161], v[200:203], v[42:45]
	s_cselect_b64 vcc, -1, 0
	v_mfma_f32_16x16x32_bf16 v[30:33], v[150:153], v[208:211], v[30:33]
	s_and_b64 s[14:15], vcc, exec
	v_mfma_f32_16x16x32_bf16 v[26:29], v[158:161], v[208:211], v[26:29]
	s_cselect_b32 s15, s55, s35
	v_mfma_f32_16x16x32_bf16 v[14:17], v[150:153], v[216:219], v[14:17]
	s_cselect_b32 s14, s54, s34
	v_mfma_f32_16x16x32_bf16 v[10:13], v[158:161], v[216:219], v[10:13]
	s_cselect_b32 s35, s69, s45
	s_setprio 0
	s_setprio 1
	v_mfma_f32_16x16x32_bf16 v[54:57], v[162:165], v[178:181], v[54:57]
	s_cselect_b32 s34, s68, s44
	v_mfma_f32_16x16x32_bf16 v[50:53], v[170:173], v[178:181], v[50:53]
	s_add_i32 s44, 0, 0x11000
	v_mfma_f32_16x16x32_bf16 v[38:41], v[162:165], v[196:199], v[38:41]
	s_add_i32 s45, 0, 0x15000
	v_mfma_f32_16x16x32_bf16 v[34:37], v[170:173], v[196:199], v[34:37]
	v_mfma_f32_16x16x32_bf16 v[22:25], v[162:165], v[204:207], v[22:25]
	v_mfma_f32_16x16x32_bf16 v[18:21], v[170:173], v[204:207], v[18:21]
	v_mfma_f32_16x16x32_bf16 v[6:9], v[162:165], v[212:215], v[6:9]
	v_mfma_f32_16x16x32_bf16 v[2:5], v[170:173], v[212:215], v[2:5]
	v_mfma_f32_16x16x32_bf16 v[54:57], v[166:169], v[182:185], v[54:57]
	v_mfma_f32_16x16x32_bf16 v[50:53], v[174:177], v[182:185], v[50:53]
	v_mfma_f32_16x16x32_bf16 v[38:41], v[166:169], v[200:203], v[38:41]
	v_mfma_f32_16x16x32_bf16 v[34:37], v[174:177], v[200:203], v[34:37]
	v_mfma_f32_16x16x32_bf16 v[22:25], v[166:169], v[208:211], v[22:25]
	v_mfma_f32_16x16x32_bf16 v[18:21], v[174:177], v[208:211], v[18:21]
	v_mfma_f32_16x16x32_bf16 v[6:9], v[166:169], v[216:219], v[6:9]
	v_mfma_f32_16x16x32_bf16 v[2:5], v[174:177], v[216:219], v[2:5]
	s_setprio 0
	s_barrier
.LBB0_391:
	v_add_u32_e32 v145, s44, v1
	ds_read_b128 v[146:149], v145
	ds_read_b128 v[150:153], v145 offset:1024
	ds_read_b128 v[154:157], v145 offset:2048
	ds_read_b128 v[158:161], v145 offset:3072
	v_add_u32_e32 v145, s45, v1
	ds_read_b128 v[162:165], v145
	ds_read_b128 v[166:169], v145 offset:1024
	ds_read_b128 v[170:173], v145 offset:2048
	ds_read_b128 v[174:177], v145 offset:3072
	v_cndmask_b32_e32 v193, v131, v141, vcc
	v_cndmask_b32_e32 v192, v130, v140, vcc
	v_lshl_add_u64 v[220:221], v[142:143], 0, s[42:43]
	v_lshl_add_u64 v[222:223], v[220:221], 0, s[6:7]
	s_add_i32 m0, s28, 0xd000
	ds_read_b128 v[178:181], v144 offset:4096
	ds_read_b128 v[182:185], v144 offset:5120
	ds_read_b128 v[196:199], v144 offset:6144
	ds_read_b128 v[200:203], v144 offset:7168
	ds_read_b128 v[204:207], v144 offset:8192
	ds_read_b128 v[208:211], v144 offset:9216
	ds_read_b128 v[212:215], v144 offset:10240
	ds_read_b128 v[216:219], v144 offset:11264
	global_load_lds_dwordx4 v[222:223], off
	v_lshl_add_u64 v[220:221], v[220:221], 0, s[8:9]
	s_add_i32 m0, s28, 0xf000
	s_nop 0
	global_load_lds_dwordx4 v[220:221], off
	s_waitcnt vmcnt(8)
	s_waitcnt lgkmcnt(0)
	s_barrier
	s_setprio 1
	s_waitcnt lgkmcnt(0)
	v_mfma_f32_16x16x32_bf16 v[126:129], v[146:149], v[178:181], v[126:129]
	v_mfma_f32_16x16x32_bf16 v[122:125], v[154:157], v[178:181], v[122:125]
	v_mfma_f32_16x16x32_bf16 v[110:113], v[146:149], v[196:199], v[110:113]
	v_mfma_f32_16x16x32_bf16 v[106:109], v[154:157], v[196:199], v[106:109]
	v_mfma_f32_16x16x32_bf16 v[94:97], v[146:149], v[204:207], v[94:97]
	v_mfma_f32_16x16x32_bf16 v[90:93], v[154:157], v[204:207], v[90:93]
	v_mfma_f32_16x16x32_bf16 v[78:81], v[146:149], v[212:215], v[78:81]
	v_mfma_f32_16x16x32_bf16 v[74:77], v[154:157], v[212:215], v[74:77]
	v_mfma_f32_16x16x32_bf16 v[126:129], v[150:153], v[182:185], v[126:129]
	v_mfma_f32_16x16x32_bf16 v[122:125], v[158:161], v[182:185], v[122:125]
	v_mfma_f32_16x16x32_bf16 v[110:113], v[150:153], v[200:203], v[110:113]
	v_mfma_f32_16x16x32_bf16 v[106:109], v[158:161], v[200:203], v[106:109]
	v_mfma_f32_16x16x32_bf16 v[94:97], v[150:153], v[208:211], v[94:97]
	v_mfma_f32_16x16x32_bf16 v[90:93], v[158:161], v[208:211], v[90:93]
	v_mfma_f32_16x16x32_bf16 v[78:81], v[150:153], v[216:219], v[78:81]
	v_mfma_f32_16x16x32_bf16 v[74:77], v[158:161], v[216:219], v[74:77]
	s_setprio 0
	s_setprio 1
	v_mfma_f32_16x16x32_bf16 v[118:121], v[162:165], v[178:181], v[118:121]
	v_mfma_f32_16x16x32_bf16 v[114:117], v[170:173], v[178:181], v[114:117]
	v_mfma_f32_16x16x32_bf16 v[102:105], v[162:165], v[196:199], v[102:105]
	v_mfma_f32_16x16x32_bf16 v[98:101], v[170:173], v[196:199], v[98:101]
	v_mfma_f32_16x16x32_bf16 v[86:89], v[162:165], v[204:207], v[86:89]
	v_mfma_f32_16x16x32_bf16 v[82:85], v[170:173], v[204:207], v[82:85]
	v_mfma_f32_16x16x32_bf16 v[70:73], v[162:165], v[212:215], v[70:73]
	v_mfma_f32_16x16x32_bf16 v[66:69], v[170:173], v[212:215], v[66:69]
	v_mfma_f32_16x16x32_bf16 v[118:121], v[166:169], v[182:185], v[118:121]
	v_mfma_f32_16x16x32_bf16 v[114:117], v[174:177], v[182:185], v[114:117]
	v_mfma_f32_16x16x32_bf16 v[102:105], v[166:169], v[200:203], v[102:105]
	v_mfma_f32_16x16x32_bf16 v[98:101], v[174:177], v[200:203], v[98:101]
	v_mfma_f32_16x16x32_bf16 v[86:89], v[166:169], v[208:211], v[86:89]
	v_mfma_f32_16x16x32_bf16 v[82:85], v[174:177], v[208:211], v[82:85]
	v_mfma_f32_16x16x32_bf16 v[70:73], v[166:169], v[216:219], v[70:73]
	v_mfma_f32_16x16x32_bf16 v[66:69], v[174:177], v[216:219], v[66:69]
	s_setprio 0
	s_barrier
	s_add_i32 s44, s44, s12
	v_lshl_add_u64 v[220:221], s[34:35], 0, v[186:187]
	s_mov_b32 m0, s44
	ds_read_b128 v[178:181], v144 offset:20480
	ds_read_b128 v[182:185], v144 offset:21504
	ds_read_b128 v[196:199], v144 offset:22528
	ds_read_b128 v[200:203], v144 offset:23552
	ds_read_b128 v[204:207], v144 offset:24576
	ds_read_b128 v[208:211], v144 offset:25600
	ds_read_b128 v[212:215], v144 offset:26624
	ds_read_b128 v[216:219], v144 offset:27648
	global_load_lds_dwordx4 v186, s[34:35]
	v_lshl_add_u64 v[222:223], v[220:221], 0, s[82:83]
	s_add_i32 m0, s44, 0x2000
	s_add_i32 s34, s45, s12
	global_load_lds_dwordx4 v[222:223], off
	v_lshl_add_u64 v[222:223], v[220:221], 0, s[64:65]
	s_mov_b32 m0, s34
	v_lshl_add_u64 v[192:193], s[14:15], 0, v[192:193]
	global_load_lds_dwordx4 v[222:223], off
	v_lshl_add_u64 v[222:223], v[220:221], 0, s[86:87]
	s_add_i32 m0, s34, 0x2000
	s_nop 0
	global_load_lds_dwordx4 v[222:223], off
	s_mov_b32 m0, s29
	v_lshl_add_u64 v[222:223], v[192:193], 0, s[82:83]
	global_load_lds_dwordx4 v[192:193], off
	s_mov_b32 m0, s47
	s_nop 0
	global_load_lds_dwordx4 v[222:223], off
	s_waitcnt vmcnt(8)
	s_waitcnt lgkmcnt(0)
	s_barrier
	s_setprio 1
	s_waitcnt lgkmcnt(0)
	v_mfma_f32_16x16x32_bf16 v[62:65], v[146:149], v[178:181], v[62:65]
	v_mfma_f32_16x16x32_bf16 v[58:61], v[154:157], v[178:181], v[58:61]
	v_mfma_f32_16x16x32_bf16 v[46:49], v[146:149], v[196:199], v[46:49]
	v_mfma_f32_16x16x32_bf16 v[42:45], v[154:157], v[196:199], v[42:45]
	v_mfma_f32_16x16x32_bf16 v[30:33], v[146:149], v[204:207], v[30:33]
	v_mfma_f32_16x16x32_bf16 v[26:29], v[154:157], v[204:207], v[26:29]
	v_mfma_f32_16x16x32_bf16 v[14:17], v[146:149], v[212:215], v[14:17]
	v_mfma_f32_16x16x32_bf16 v[10:13], v[154:157], v[212:215], v[10:13]
	v_mfma_f32_16x16x32_bf16 v[62:65], v[150:153], v[182:185], v[62:65]
	v_mfma_f32_16x16x32_bf16 v[58:61], v[158:161], v[182:185], v[58:61]
	v_mfma_f32_16x16x32_bf16 v[46:49], v[150:153], v[200:203], v[46:49]
	v_mfma_f32_16x16x32_bf16 v[42:45], v[158:161], v[200:203], v[42:45]
	v_mfma_f32_16x16x32_bf16 v[30:33], v[150:153], v[208:211], v[30:33]
	v_mfma_f32_16x16x32_bf16 v[26:29], v[158:161], v[208:211], v[26:29]
	v_mfma_f32_16x16x32_bf16 v[14:17], v[150:153], v[216:219], v[14:17]
	v_mfma_f32_16x16x32_bf16 v[10:13], v[158:161], v[216:219], v[10:13]
	s_setprio 0
	s_setprio 1
	v_mfma_f32_16x16x32_bf16 v[54:57], v[162:165], v[178:181], v[54:57]
	v_mfma_f32_16x16x32_bf16 v[50:53], v[170:173], v[178:181], v[50:53]
	v_mfma_f32_16x16x32_bf16 v[38:41], v[162:165], v[196:199], v[38:41]
	v_mfma_f32_16x16x32_bf16 v[34:37], v[170:173], v[196:199], v[34:37]
	v_mfma_f32_16x16x32_bf16 v[22:25], v[162:165], v[204:207], v[22:25]
	v_mfma_f32_16x16x32_bf16 v[18:21], v[170:173], v[204:207], v[18:21]
	v_mfma_f32_16x16x32_bf16 v[6:9], v[162:165], v[212:215], v[6:9]
	v_mfma_f32_16x16x32_bf16 v[2:5], v[170:173], v[212:215], v[2:5]
	v_mfma_f32_16x16x32_bf16 v[54:57], v[166:169], v[182:185], v[54:57]
	v_mfma_f32_16x16x32_bf16 v[50:53], v[174:177], v[182:185], v[50:53]
	v_mfma_f32_16x16x32_bf16 v[38:41], v[166:169], v[200:203], v[38:41]
	v_mfma_f32_16x16x32_bf16 v[34:37], v[174:177], v[200:203], v[34:37]
	v_mfma_f32_16x16x32_bf16 v[22:25], v[166:169], v[208:211], v[22:25]
	v_mfma_f32_16x16x32_bf16 v[18:21], v[174:177], v[208:211], v[18:21]
	v_mfma_f32_16x16x32_bf16 v[6:9], v[166:169], v[216:219], v[6:9]
	v_mfma_f32_16x16x32_bf16 v[2:5], v[174:177], v[216:219], v[2:5]
	s_setprio 0
	s_barrier
	s_add_i32 s14, 0, 0x19000
	v_add_u32_e32 v145, s14, v1
	s_add_i32 s15, 0, 0x1d000
	ds_read_b128 v[146:149], v145
	ds_read_b128 v[150:153], v145 offset:1024
	ds_read_b128 v[154:157], v145 offset:2048
	ds_read_b128 v[158:161], v145 offset:3072
	v_add_u32_e32 v145, s15, v1
	ds_read_b128 v[162:165], v145
	ds_read_b128 v[166:169], v145 offset:1024
	ds_read_b128 v[170:173], v145 offset:2048
	ds_read_b128 v[174:177], v145 offset:3072
	s_mov_b32 m0, s60
	v_lshl_add_u64 v[222:223], v[192:193], 0, s[64:65]
	ds_read_b128 v[178:181], v144 offset:36864
	ds_read_b128 v[182:185], v144 offset:37888
	ds_read_b128 v[196:199], v144 offset:38912
	ds_read_b128 v[200:203], v144 offset:39936
	ds_read_b128 v[204:207], v144 offset:40960
	ds_read_b128 v[208:211], v144 offset:41984
	ds_read_b128 v[212:215], v144 offset:43008
	ds_read_b128 v[216:219], v144 offset:44032
	global_load_lds_dwordx4 v[222:223], off
	v_lshl_add_u64 v[222:223], v[192:193], 0, s[86:87]
	s_mov_b32 m0, s61
	s_nop 0
	global_load_lds_dwordx4 v[222:223], off
	s_waitcnt vmcnt(8)
	s_waitcnt lgkmcnt(0)
	s_barrier
	s_setprio 1
	s_waitcnt lgkmcnt(0)
	v_mfma_f32_16x16x32_bf16 v[126:129], v[146:149], v[178:181], v[126:129]
	v_mfma_f32_16x16x32_bf16 v[122:125], v[154:157], v[178:181], v[122:125]
	v_mfma_f32_16x16x32_bf16 v[110:113], v[146:149], v[196:199], v[110:113]
	v_mfma_f32_16x16x32_bf16 v[106:109], v[154:157], v[196:199], v[106:109]
	v_mfma_f32_16x16x32_bf16 v[94:97], v[146:149], v[204:207], v[94:97]
	v_mfma_f32_16x16x32_bf16 v[90:93], v[154:157], v[204:207], v[90:93]
	v_mfma_f32_16x16x32_bf16 v[78:81], v[146:149], v[212:215], v[78:81]
	v_mfma_f32_16x16x32_bf16 v[74:77], v[154:157], v[212:215], v[74:77]
	v_mfma_f32_16x16x32_bf16 v[126:129], v[150:153], v[182:185], v[126:129]
	v_mfma_f32_16x16x32_bf16 v[122:125], v[158:161], v[182:185], v[122:125]
	v_mfma_f32_16x16x32_bf16 v[110:113], v[150:153], v[200:203], v[110:113]
	v_mfma_f32_16x16x32_bf16 v[106:109], v[158:161], v[200:203], v[106:109]
	v_mfma_f32_16x16x32_bf16 v[94:97], v[150:153], v[208:211], v[94:97]
	v_mfma_f32_16x16x32_bf16 v[90:93], v[158:161], v[208:211], v[90:93]
	v_mfma_f32_16x16x32_bf16 v[78:81], v[150:153], v[216:219], v[78:81]
	v_mfma_f32_16x16x32_bf16 v[74:77], v[158:161], v[216:219], v[74:77]
	s_setprio 0
	s_setprio 1
	v_mfma_f32_16x16x32_bf16 v[118:121], v[162:165], v[178:181], v[118:121]
	v_mfma_f32_16x16x32_bf16 v[114:117], v[170:173], v[178:181], v[114:117]
	v_mfma_f32_16x16x32_bf16 v[102:105], v[162:165], v[196:199], v[102:105]
	v_mfma_f32_16x16x32_bf16 v[98:101], v[170:173], v[196:199], v[98:101]
	v_mfma_f32_16x16x32_bf16 v[86:89], v[162:165], v[204:207], v[86:89]
	v_mfma_f32_16x16x32_bf16 v[82:85], v[170:173], v[204:207], v[82:85]
	v_mfma_f32_16x16x32_bf16 v[70:73], v[162:165], v[212:215], v[70:73]
	v_mfma_f32_16x16x32_bf16 v[66:69], v[170:173], v[212:215], v[66:69]
	v_mfma_f32_16x16x32_bf16 v[118:121], v[166:169], v[182:185], v[118:121]
	v_mfma_f32_16x16x32_bf16 v[114:117], v[174:177], v[182:185], v[114:117]
	v_mfma_f32_16x16x32_bf16 v[102:105], v[166:169], v[200:203], v[102:105]
	v_mfma_f32_16x16x32_bf16 v[98:101], v[174:177], v[200:203], v[98:101]
	v_mfma_f32_16x16x32_bf16 v[86:89], v[166:169], v[208:211], v[86:89]
	v_mfma_f32_16x16x32_bf16 v[82:85], v[174:177], v[208:211], v[82:85]
	v_mfma_f32_16x16x32_bf16 v[70:73], v[166:169], v[216:219], v[70:73]
	v_mfma_f32_16x16x32_bf16 v[66:69], v[174:177], v[216:219], v[66:69]
	s_setprio 0
	s_barrier
	s_add_i32 s14, s14, s12
	v_lshl_add_u64 v[222:223], v[220:221], 0, s[92:93]
	s_mov_b32 m0, s14
	ds_read_b128 v[178:181], v144 offset:53248
	ds_read_b128 v[182:185], v144 offset:54272
	ds_read_b128 v[196:199], v144 offset:55296
	ds_read_b128 v[200:203], v144 offset:56320
	ds_read_b128 v[204:207], v144 offset:57344
	ds_read_b128 v[208:211], v144 offset:58368
	ds_read_b128 v[212:215], v144 offset:59392
	ds_read_b128 v[216:219], v144 offset:60416
	global_load_lds_dwordx4 v[222:223], off
	v_lshl_add_u64 v[222:223], v[220:221], 0, s[4:5]
	s_add_i32 m0, s14, 0x2000
	s_add_i32 s14, s15, s12
	global_load_lds_dwordx4 v[222:223], off
	v_lshl_add_u64 v[222:223], v[220:221], 0, s[6:7]
	s_mov_b32 m0, s14
	v_lshl_add_u64 v[220:221], v[220:221], 0, s[8:9]
	global_load_lds_dwordx4 v[222:223], off
	s_add_i32 m0, s14, 0x2000
	s_nop 0
	global_load_lds_dwordx4 v[220:221], off
	v_lshl_add_u64 v[220:221], v[192:193], 0, s[92:93]
	s_mov_b32 m0, s76
	v_lshl_add_u64 v[192:193], v[192:193], 0, s[4:5]
	global_load_lds_dwordx4 v[220:221], off
	s_mov_b32 m0, s77
	s_nop 0
	global_load_lds_dwordx4 v[192:193], off
	s_waitcnt vmcnt(8)
	s_waitcnt lgkmcnt(0)
	s_barrier
	s_setprio 1
	s_waitcnt lgkmcnt(0)
	v_mfma_f32_16x16x32_bf16 v[62:65], v[146:149], v[178:181], v[62:65]
	v_mfma_f32_16x16x32_bf16 v[58:61], v[154:157], v[178:181], v[58:61]
	s_add_i32 s25, s25, 2
	v_mfma_f32_16x16x32_bf16 v[46:49], v[146:149], v[196:199], v[46:49]
	s_add_u32 s42, s42, 0x100
	v_mfma_f32_16x16x32_bf16 v[42:45], v[154:157], v[196:199], v[42:45]
	s_addc_u32 s43, s43, 0
	v_mfma_f32_16x16x32_bf16 v[30:33], v[146:149], v[204:207], v[30:33]
	s_add_u32 s14, s40, s42
	v_mfma_f32_16x16x32_bf16 v[26:29], v[154:157], v[204:207], v[26:29]
	s_addc_u32 s15, s41, s43
	v_mfma_f32_16x16x32_bf16 v[14:17], v[146:149], v[212:215], v[14:17]
	s_add_u32 s34, s14, 0x100
	v_mfma_f32_16x16x32_bf16 v[10:13], v[154:157], v[212:215], v[10:13]
	s_addc_u32 s35, s15, 0
	v_mfma_f32_16x16x32_bf16 v[62:65], v[150:153], v[182:185], v[62:65]
	s_add_u32 s44, s1, s42
	v_mfma_f32_16x16x32_bf16 v[58:61], v[158:161], v[182:185], v[58:61]
	s_addc_u32 s45, s24, s43
	v_mfma_f32_16x16x32_bf16 v[46:49], v[150:153], v[200:203], v[46:49]
	s_cmpk_eq_i32 s42, 0x700
	v_mfma_f32_16x16x32_bf16 v[42:45], v[158:161], v[200:203], v[42:45]
	s_cselect_b64 vcc, -1, 0
	v_mfma_f32_16x16x32_bf16 v[30:33], v[150:153], v[208:211], v[30:33]
	s_and_b64 s[14:15], vcc, exec
	v_mfma_f32_16x16x32_bf16 v[26:29], v[158:161], v[208:211], v[26:29]
	s_cselect_b32 s15, s55, s35
	v_mfma_f32_16x16x32_bf16 v[14:17], v[150:153], v[216:219], v[14:17]
	s_cselect_b32 s14, s54, s34
	v_mfma_f32_16x16x32_bf16 v[10:13], v[158:161], v[216:219], v[10:13]
	s_cselect_b32 s35, s69, s45
	s_setprio 0
	s_setprio 1
	v_mfma_f32_16x16x32_bf16 v[54:57], v[162:165], v[178:181], v[54:57]
	s_cselect_b32 s34, s68, s44
	v_mfma_f32_16x16x32_bf16 v[50:53], v[170:173], v[178:181], v[50:53]
	s_add_i32 s44, 0, 0x11000
	v_mfma_f32_16x16x32_bf16 v[38:41], v[162:165], v[196:199], v[38:41]
	s_add_i32 s45, 0, 0x15000
	v_mfma_f32_16x16x32_bf16 v[34:37], v[170:173], v[196:199], v[34:37]
	v_mfma_f32_16x16x32_bf16 v[22:25], v[162:165], v[204:207], v[22:25]
	v_mfma_f32_16x16x32_bf16 v[18:21], v[170:173], v[204:207], v[18:21]
	v_mfma_f32_16x16x32_bf16 v[6:9], v[162:165], v[212:215], v[6:9]
	v_mfma_f32_16x16x32_bf16 v[2:5], v[170:173], v[212:215], v[2:5]
	v_mfma_f32_16x16x32_bf16 v[54:57], v[166:169], v[182:185], v[54:57]
	v_mfma_f32_16x16x32_bf16 v[50:53], v[174:177], v[182:185], v[50:53]
	v_mfma_f32_16x16x32_bf16 v[38:41], v[166:169], v[200:203], v[38:41]
	v_mfma_f32_16x16x32_bf16 v[34:37], v[174:177], v[200:203], v[34:37]
	v_mfma_f32_16x16x32_bf16 v[22:25], v[166:169], v[208:211], v[22:25]
	v_mfma_f32_16x16x32_bf16 v[18:21], v[174:177], v[208:211], v[18:21]
	v_mfma_f32_16x16x32_bf16 v[6:9], v[166:169], v[216:219], v[6:9]
	v_mfma_f32_16x16x32_bf16 v[2:5], v[174:177], v[216:219], v[2:5]
	s_setprio 0
	s_barrier
	s_cmp_gt_u32 s25, 13
	s_cbranch_scc0 .LBB0_391
	s_and_b64 vcc, exec, s[50:51]
	s_cbranch_vccz .LBB0_394
	s_barrier

.LBB0_1110:
	s_add_u32 s24, s54, 0x100
	v_lshl_add_u64 v[140:141], s[52:53], 0, v[138:139]
	s_addc_u32 s25, s55, 0
	s_mov_b32 s43, -2
	s_mov_b64 s[54:55], 0
	s_add_u32 s14, s52, s54
	s_addc_u32 s15, s53, s55
	s_add_u32 s45, s14, 0x100
	s_addc_u32 s73, s15, 0
	s_add_u32 s74, s24, s54
	s_addc_u32 s75, s25, s55
	s_cmpk_eq_i32 s54, 0x700
	s_cselect_b64 vcc, -1, 0
	s_and_b64 s[14:15], vcc, exec
	s_cselect_b32 s15, s47, s73
	s_cselect_b32 s14, s46, s45
	s_cselect_b32 s75, s49, s75
	s_cselect_b32 s74, s48, s74
	s_add_i32 s45, 0, 0x11000
	v_add_u32_e32 v131, s45, v1
	s_add_i32 s73, 0, 0x15000
	ds_read_b128 v[144:147], v131
	ds_read_b128 v[148:151], v131 offset:1024
	ds_read_b128 v[152:155], v131 offset:2048
	ds_read_b128 v[156:159], v131 offset:3072
	v_add_u32_e32 v131, s73, v1
	ds_read_b128 v[160:163], v131
	ds_read_b128 v[164:167], v131 offset:1024
	ds_read_b128 v[168:171], v131 offset:2048
	ds_read_b128 v[172:175], v131 offset:3072
	v_cndmask_b32_e32 v185, v139, v137, vcc
	v_cndmask_b32_e32 v184, v138, v136, vcc
	v_lshl_add_u64 v[192:193], v[140:141], 0, s[54:55]
	v_lshl_add_u64 v[220:221], v[192:193], 0, s[6:7]
	s_add_i32 m0, s29, 0xd000
	ds_read_b128 v[176:179], v142 offset:4096
	ds_read_b128 v[180:183], v142 offset:5120
	ds_read_b128 v[196:199], v142 offset:6144
	ds_read_b128 v[200:203], v142 offset:7168
	ds_read_b128 v[204:207], v142 offset:8192
	ds_read_b128 v[208:211], v142 offset:9216
	ds_read_b128 v[212:215], v142 offset:10240
	ds_read_b128 v[216:219], v142 offset:11264
	global_load_lds_dwordx4 v[220:221], off
	v_lshl_add_u64 v[192:193], v[192:193], 0, s[8:9]
	s_add_i32 m0, s29, 0xf000
	s_nop 0
	global_load_lds_dwordx4 v[192:193], off
	s_waitcnt vmcnt(8)
	s_waitcnt lgkmcnt(0)
	s_barrier
	s_setprio 1
	s_waitcnt lgkmcnt(0)
	v_mfma_f32_16x16x32_bf16 v[126:129], v[144:147], v[176:179], 0
	v_mfma_f32_16x16x32_bf16 v[122:125], v[152:155], v[176:179], 0
	v_mfma_f32_16x16x32_bf16 v[110:113], v[144:147], v[196:199], 0
	v_mfma_f32_16x16x32_bf16 v[106:109], v[152:155], v[196:199], 0
	v_mfma_f32_16x16x32_bf16 v[94:97], v[144:147], v[204:207], 0
	v_mfma_f32_16x16x32_bf16 v[90:93], v[152:155], v[204:207], 0
	v_mfma_f32_16x16x32_bf16 v[78:81], v[144:147], v[212:215], 0
	v_mfma_f32_16x16x32_bf16 v[74:77], v[152:155], v[212:215], 0
	v_mfma_f32_16x16x32_bf16 v[126:129], v[148:151], v[180:183], v[126:129]
	v_mfma_f32_16x16x32_bf16 v[122:125], v[156:159], v[180:183], v[122:125]
	v_mfma_f32_16x16x32_bf16 v[110:113], v[148:151], v[200:203], v[110:113]
	v_mfma_f32_16x16x32_bf16 v[106:109], v[156:159], v[200:203], v[106:109]
	v_mfma_f32_16x16x32_bf16 v[94:97], v[148:151], v[208:211], v[94:97]
	v_mfma_f32_16x16x32_bf16 v[90:93], v[156:159], v[208:211], v[90:93]
	v_mfma_f32_16x16x32_bf16 v[78:81], v[148:151], v[216:219], v[78:81]
	v_mfma_f32_16x16x32_bf16 v[74:77], v[156:159], v[216:219], v[74:77]
	s_setprio 0
	s_setprio 1
	v_mfma_f32_16x16x32_bf16 v[118:121], v[160:163], v[176:179], 0
	v_mfma_f32_16x16x32_bf16 v[114:117], v[168:171], v[176:179], 0
	v_mfma_f32_16x16x32_bf16 v[102:105], v[160:163], v[196:199], 0
	v_mfma_f32_16x16x32_bf16 v[98:101], v[168:171], v[196:199], 0
	v_mfma_f32_16x16x32_bf16 v[86:89], v[160:163], v[204:207], 0
	v_mfma_f32_16x16x32_bf16 v[82:85], v[168:171], v[204:207], 0
	v_mfma_f32_16x16x32_bf16 v[70:73], v[160:163], v[212:215], 0
	v_mfma_f32_16x16x32_bf16 v[66:69], v[168:171], v[212:215], 0
	v_mfma_f32_16x16x32_bf16 v[118:121], v[164:167], v[180:183], v[118:121]
	v_mfma_f32_16x16x32_bf16 v[114:117], v[172:175], v[180:183], v[114:117]
	v_mfma_f32_16x16x32_bf16 v[102:105], v[164:167], v[200:203], v[102:105]
	v_mfma_f32_16x16x32_bf16 v[98:101], v[172:175], v[200:203], v[98:101]
	v_mfma_f32_16x16x32_bf16 v[86:89], v[164:167], v[208:211], v[86:89]
	v_mfma_f32_16x16x32_bf16 v[82:85], v[172:175], v[208:211], v[82:85]
	v_mfma_f32_16x16x32_bf16 v[70:73], v[164:167], v[216:219], v[70:73]
	v_mfma_f32_16x16x32_bf16 v[66:69], v[172:175], v[216:219], v[66:69]
	s_setprio 0
	s_barrier
	s_add_i32 s45, s45, s2
	v_lshl_add_u64 v[192:193], s[74:75], 0, v[186:187]
	s_mov_b32 m0, s45
	ds_read_b128 v[176:179], v142 offset:20480
	ds_read_b128 v[180:183], v142 offset:21504
	ds_read_b128 v[196:199], v142 offset:22528
	ds_read_b128 v[200:203], v142 offset:23552
	ds_read_b128 v[204:207], v142 offset:24576
	ds_read_b128 v[208:211], v142 offset:25600
	ds_read_b128 v[212:215], v142 offset:26624
	ds_read_b128 v[216:219], v142 offset:27648
	global_load_lds_dwordx4 v186, s[74:75]
	v_lshl_add_u64 v[220:221], v[192:193], 0, s[82:83]
	s_add_i32 m0, s45, 0x2000
	s_add_i32 s45, s73, s2
	global_load_lds_dwordx4 v[220:221], off
	v_lshl_add_u64 v[220:221], v[192:193], 0, s[64:65]
	s_mov_b32 m0, s45
	v_lshl_add_u64 v[184:185], s[14:15], 0, v[184:185]
	global_load_lds_dwordx4 v[220:221], off
	v_lshl_add_u64 v[220:221], v[192:193], 0, s[86:87]
	s_add_i32 m0, s45, 0x2000
	s_nop 0
	global_load_lds_dwordx4 v[220:221], off
	s_mov_b32 m0, s33
	v_lshl_add_u64 v[220:221], v[184:185], 0, s[82:83]
	global_load_lds_dwordx4 v[184:185], off
	s_mov_b32 m0, s34
	s_nop 0
	global_load_lds_dwordx4 v[220:221], off
	s_waitcnt vmcnt(8)
	s_waitcnt lgkmcnt(0)
	s_barrier
	s_setprio 1
	s_waitcnt lgkmcnt(0)
	v_mfma_f32_16x16x32_bf16 v[62:65], v[144:147], v[176:179], 0
	v_mfma_f32_16x16x32_bf16 v[58:61], v[152:155], v[176:179], 0
	v_mfma_f32_16x16x32_bf16 v[46:49], v[144:147], v[196:199], 0
	v_mfma_f32_16x16x32_bf16 v[42:45], v[152:155], v[196:199], 0
	v_mfma_f32_16x16x32_bf16 v[30:33], v[144:147], v[204:207], 0
	v_mfma_f32_16x16x32_bf16 v[26:29], v[152:155], v[204:207], 0
	v_mfma_f32_16x16x32_bf16 v[14:17], v[144:147], v[212:215], 0
	v_mfma_f32_16x16x32_bf16 v[10:13], v[152:155], v[212:215], 0
	v_mfma_f32_16x16x32_bf16 v[62:65], v[148:151], v[180:183], v[62:65]
	v_mfma_f32_16x16x32_bf16 v[58:61], v[156:159], v[180:183], v[58:61]
	v_mfma_f32_16x16x32_bf16 v[46:49], v[148:151], v[200:203], v[46:49]
	v_mfma_f32_16x16x32_bf16 v[42:45], v[156:159], v[200:203], v[42:45]
	v_mfma_f32_16x16x32_bf16 v[30:33], v[148:151], v[208:211], v[30:33]
	v_mfma_f32_16x16x32_bf16 v[26:29], v[156:159], v[208:211], v[26:29]
	v_mfma_f32_16x16x32_bf16 v[14:17], v[148:151], v[216:219], v[14:17]
	v_mfma_f32_16x16x32_bf16 v[10:13], v[156:159], v[216:219], v[10:13]
	s_setprio 0
	s_setprio 1
	v_mfma_f32_16x16x32_bf16 v[54:57], v[160:163], v[176:179], 0
	v_mfma_f32_16x16x32_bf16 v[50:53], v[168:171], v[176:179], 0
	v_mfma_f32_16x16x32_bf16 v[38:41], v[160:163], v[196:199], 0
	v_mfma_f32_16x16x32_bf16 v[34:37], v[168:171], v[196:199], 0
	v_mfma_f32_16x16x32_bf16 v[22:25], v[160:163], v[204:207], 0
	v_mfma_f32_16x16x32_bf16 v[18:21], v[168:171], v[204:207], 0
	v_mfma_f32_16x16x32_bf16 v[6:9], v[160:163], v[212:215], 0
	v_mfma_f32_16x16x32_bf16 v[2:5], v[168:171], v[212:215], 0
	v_mfma_f32_16x16x32_bf16 v[54:57], v[164:167], v[180:183], v[54:57]
	v_mfma_f32_16x16x32_bf16 v[50:53], v[172:175], v[180:183], v[50:53]
	v_mfma_f32_16x16x32_bf16 v[38:41], v[164:167], v[200:203], v[38:41]
	v_mfma_f32_16x16x32_bf16 v[34:37], v[172:175], v[200:203], v[34:37]
	v_mfma_f32_16x16x32_bf16 v[22:25], v[164:167], v[208:211], v[22:25]
	v_mfma_f32_16x16x32_bf16 v[18:21], v[172:175], v[208:211], v[18:21]
	v_mfma_f32_16x16x32_bf16 v[6:9], v[164:167], v[216:219], v[6:9]
	v_mfma_f32_16x16x32_bf16 v[2:5], v[172:175], v[216:219], v[2:5]
	s_setprio 0
	s_barrier
	s_add_i32 s14, 0, 0x19000
	v_add_u32_e32 v131, s14, v1
	s_add_i32 s15, 0, 0x1d000
	ds_read_b128 v[144:147], v131
	ds_read_b128 v[148:151], v131 offset:1024
	ds_read_b128 v[152:155], v131 offset:2048
	ds_read_b128 v[156:159], v131 offset:3072
	v_add_u32_e32 v131, s15, v1
	ds_read_b128 v[160:163], v131
	ds_read_b128 v[164:167], v131 offset:1024
	ds_read_b128 v[168:171], v131 offset:2048
	ds_read_b128 v[172:175], v131 offset:3072
	s_mov_b32 m0, s35
	v_lshl_add_u64 v[220:221], v[184:185], 0, s[64:65]
	ds_read_b128 v[176:179], v142 offset:36864
	ds_read_b128 v[180:183], v142 offset:37888
	ds_read_b128 v[196:199], v142 offset:38912
	ds_read_b128 v[200:203], v142 offset:39936
	ds_read_b128 v[204:207], v142 offset:40960
	ds_read_b128 v[208:211], v142 offset:41984
	ds_read_b128 v[212:215], v142 offset:43008
	ds_read_b128 v[216:219], v142 offset:44032
	global_load_lds_dwordx4 v[220:221], off
	v_lshl_add_u64 v[220:221], v[184:185], 0, s[86:87]
	s_mov_b32 m0, s56
	s_nop 0
	global_load_lds_dwordx4 v[220:221], off
	s_waitcnt vmcnt(8)
	s_waitcnt lgkmcnt(0)
	s_barrier
	s_setprio 1
	s_waitcnt lgkmcnt(0)
	v_mfma_f32_16x16x32_bf16 v[126:129], v[144:147], v[176:179], v[126:129]
	v_mfma_f32_16x16x32_bf16 v[122:125], v[152:155], v[176:179], v[122:125]
	v_mfma_f32_16x16x32_bf16 v[110:113], v[144:147], v[196:199], v[110:113]
	v_mfma_f32_16x16x32_bf16 v[106:109], v[152:155], v[196:199], v[106:109]
	v_mfma_f32_16x16x32_bf16 v[94:97], v[144:147], v[204:207], v[94:97]
	v_mfma_f32_16x16x32_bf16 v[90:93], v[152:155], v[204:207], v[90:93]
	v_mfma_f32_16x16x32_bf16 v[78:81], v[144:147], v[212:215], v[78:81]
	v_mfma_f32_16x16x32_bf16 v[74:77], v[152:155], v[212:215], v[74:77]
	v_mfma_f32_16x16x32_bf16 v[126:129], v[148:151], v[180:183], v[126:129]
	v_mfma_f32_16x16x32_bf16 v[122:125], v[156:159], v[180:183], v[122:125]
	v_mfma_f32_16x16x32_bf16 v[110:113], v[148:151], v[200:203], v[110:113]
	v_mfma_f32_16x16x32_bf16 v[106:109], v[156:159], v[200:203], v[106:109]
	v_mfma_f32_16x16x32_bf16 v[94:97], v[148:151], v[208:211], v[94:97]
	v_mfma_f32_16x16x32_bf16 v[90:93], v[156:159], v[208:211], v[90:93]
	v_mfma_f32_16x16x32_bf16 v[78:81], v[148:151], v[216:219], v[78:81]
	v_mfma_f32_16x16x32_bf16 v[74:77], v[156:159], v[216:219], v[74:77]
	s_setprio 0
	s_setprio 1
	v_mfma_f32_16x16x32_bf16 v[118:121], v[160:163], v[176:179], v[118:121]
	v_mfma_f32_16x16x32_bf16 v[114:117], v[168:171], v[176:179], v[114:117]
	v_mfma_f32_16x16x32_bf16 v[102:105], v[160:163], v[196:199], v[102:105]
	v_mfma_f32_16x16x32_bf16 v[98:101], v[168:171], v[196:199], v[98:101]
	v_mfma_f32_16x16x32_bf16 v[86:89], v[160:163], v[204:207], v[86:89]
	v_mfma_f32_16x16x32_bf16 v[82:85], v[168:171], v[204:207], v[82:85]
	v_mfma_f32_16x16x32_bf16 v[70:73], v[160:163], v[212:215], v[70:73]
	v_mfma_f32_16x16x32_bf16 v[66:69], v[168:171], v[212:215], v[66:69]
	v_mfma_f32_16x16x32_bf16 v[118:121], v[164:167], v[180:183], v[118:121]
	v_mfma_f32_16x16x32_bf16 v[114:117], v[172:175], v[180:183], v[114:117]
	v_mfma_f32_16x16x32_bf16 v[102:105], v[164:167], v[200:203], v[102:105]
	v_mfma_f32_16x16x32_bf16 v[98:101], v[172:175], v[200:203], v[98:101]
	v_mfma_f32_16x16x32_bf16 v[86:89], v[164:167], v[208:211], v[86:89]
	v_mfma_f32_16x16x32_bf16 v[82:85], v[172:175], v[208:211], v[82:85]
	v_mfma_f32_16x16x32_bf16 v[70:73], v[164:167], v[216:219], v[70:73]
	v_mfma_f32_16x16x32_bf16 v[66:69], v[172:175], v[216:219], v[66:69]
	s_setprio 0
	s_barrier
	s_add_i32 s14, s14, s2
	v_lshl_add_u64 v[220:221], v[192:193], 0, s[92:93]
	s_mov_b32 m0, s14
	ds_read_b128 v[176:179], v142 offset:53248
	ds_read_b128 v[180:183], v142 offset:54272
	ds_read_b128 v[196:199], v142 offset:55296
	ds_read_b128 v[200:203], v142 offset:56320
	ds_read_b128 v[204:207], v142 offset:57344
	ds_read_b128 v[208:211], v142 offset:58368
	ds_read_b128 v[212:215], v142 offset:59392
	ds_read_b128 v[216:219], v142 offset:60416
	global_load_lds_dwordx4 v[220:221], off
	v_lshl_add_u64 v[220:221], v[192:193], 0, s[4:5]
	s_add_i32 m0, s14, 0x2000
	s_add_i32 s14, s15, s2
	global_load_lds_dwordx4 v[220:221], off
	v_lshl_add_u64 v[220:221], v[192:193], 0, s[6:7]
	s_mov_b32 m0, s14
	v_lshl_add_u64 v[192:193], v[192:193], 0, s[8:9]
	global_load_lds_dwordx4 v[220:221], off
	s_add_i32 m0, s14, 0x2000
	s_nop 0
	global_load_lds_dwordx4 v[192:193], off
	v_lshl_add_u64 v[192:193], v[184:185], 0, s[92:93]
	s_mov_b32 m0, s59
	v_lshl_add_u64 v[184:185], v[184:185], 0, s[4:5]
	global_load_lds_dwordx4 v[192:193], off
	s_mov_b32 m0, s60
	s_nop 0
	global_load_lds_dwordx4 v[184:185], off
	s_waitcnt vmcnt(8)
	s_waitcnt lgkmcnt(0)
	s_barrier
	s_setprio 1
	s_waitcnt lgkmcnt(0)
	v_mfma_f32_16x16x32_bf16 v[62:65], v[144:147], v[176:179], v[62:65]
	v_mfma_f32_16x16x32_bf16 v[58:61], v[152:155], v[176:179], v[58:61]
	s_add_i32 s43, s43, 2
	v_mfma_f32_16x16x32_bf16 v[46:49], v[144:147], v[196:199], v[46:49]
	s_add_u32 s54, s54, 0x100
	v_mfma_f32_16x16x32_bf16 v[42:45], v[152:155], v[196:199], v[42:45]
	s_addc_u32 s55, s55, 0
	v_mfma_f32_16x16x32_bf16 v[30:33], v[144:147], v[204:207], v[30:33]
	s_add_u32 s14, s52, s54
	v_mfma_f32_16x16x32_bf16 v[26:29], v[152:155], v[204:207], v[26:29]
	s_addc_u32 s15, s53, s55
	v_mfma_f32_16x16x32_bf16 v[14:17], v[144:147], v[212:215], v[14:17]
	s_add_u32 s45, s14, 0x100
	v_mfma_f32_16x16x32_bf16 v[10:13], v[152:155], v[212:215], v[10:13]
	s_addc_u32 s73, s15, 0
	v_mfma_f32_16x16x32_bf16 v[62:65], v[148:151], v[180:183], v[62:65]
	s_add_u32 s74, s24, s54
	v_mfma_f32_16x16x32_bf16 v[58:61], v[156:159], v[180:183], v[58:61]
	s_addc_u32 s75, s25, s55
	v_mfma_f32_16x16x32_bf16 v[46:49], v[148:151], v[200:203], v[46:49]
	s_cmpk_eq_i32 s54, 0x700
	v_mfma_f32_16x16x32_bf16 v[42:45], v[156:159], v[200:203], v[42:45]
	s_cselect_b64 vcc, -1, 0
	v_mfma_f32_16x16x32_bf16 v[30:33], v[148:151], v[208:211], v[30:33]
	s_and_b64 s[14:15], vcc, exec
	v_mfma_f32_16x16x32_bf16 v[26:29], v[156:159], v[208:211], v[26:29]
	s_cselect_b32 s15, s47, s73
	v_mfma_f32_16x16x32_bf16 v[14:17], v[148:151], v[216:219], v[14:17]
	s_cselect_b32 s14, s46, s45
	v_mfma_f32_16x16x32_bf16 v[10:13], v[156:159], v[216:219], v[10:13]
	s_cselect_b32 s75, s49, s75
	s_setprio 0
	s_setprio 1
	v_mfma_f32_16x16x32_bf16 v[54:57], v[160:163], v[176:179], v[54:57]
	s_cselect_b32 s74, s48, s74
	v_mfma_f32_16x16x32_bf16 v[50:53], v[168:171], v[176:179], v[50:53]
	s_add_i32 s45, 0, 0x11000
	v_mfma_f32_16x16x32_bf16 v[38:41], v[160:163], v[196:199], v[38:41]
	s_add_i32 s73, 0, 0x15000
	v_mfma_f32_16x16x32_bf16 v[34:37], v[168:171], v[196:199], v[34:37]
	v_mfma_f32_16x16x32_bf16 v[22:25], v[160:163], v[204:207], v[22:25]
	v_mfma_f32_16x16x32_bf16 v[18:21], v[168:171], v[204:207], v[18:21]
	v_mfma_f32_16x16x32_bf16 v[6:9], v[160:163], v[212:215], v[6:9]
	v_mfma_f32_16x16x32_bf16 v[2:5], v[168:171], v[212:215], v[2:5]
	v_mfma_f32_16x16x32_bf16 v[54:57], v[164:167], v[180:183], v[54:57]
	v_mfma_f32_16x16x32_bf16 v[50:53], v[172:175], v[180:183], v[50:53]
	v_mfma_f32_16x16x32_bf16 v[38:41], v[164:167], v[200:203], v[38:41]
	v_mfma_f32_16x16x32_bf16 v[34:37], v[172:175], v[200:203], v[34:37]
	v_mfma_f32_16x16x32_bf16 v[22:25], v[164:167], v[208:211], v[22:25]
	v_mfma_f32_16x16x32_bf16 v[18:21], v[172:175], v[208:211], v[18:21]
	v_mfma_f32_16x16x32_bf16 v[6:9], v[164:167], v[216:219], v[6:9]
	v_mfma_f32_16x16x32_bf16 v[2:5], v[172:175], v[216:219], v[2:5]
	s_setprio 0
	s_barrier
.LBB0_1111:
	v_add_u32_e32 v131, s45, v1
	ds_read_b128 v[144:147], v131
	ds_read_b128 v[148:151], v131 offset:1024
	ds_read_b128 v[152:155], v131 offset:2048
	ds_read_b128 v[156:159], v131 offset:3072
	v_add_u32_e32 v131, s73, v1
	ds_read_b128 v[160:163], v131
	ds_read_b128 v[164:167], v131 offset:1024
	ds_read_b128 v[168:171], v131 offset:2048
	ds_read_b128 v[172:175], v131 offset:3072
	v_cndmask_b32_e32 v185, v139, v137, vcc
	v_cndmask_b32_e32 v184, v138, v136, vcc
	v_lshl_add_u64 v[192:193], v[140:141], 0, s[54:55]
	v_lshl_add_u64 v[220:221], v[192:193], 0, s[6:7]
	s_add_i32 m0, s29, 0xd000
	ds_read_b128 v[176:179], v142 offset:4096
	ds_read_b128 v[180:183], v142 offset:5120
	ds_read_b128 v[196:199], v142 offset:6144
	ds_read_b128 v[200:203], v142 offset:7168
	ds_read_b128 v[204:207], v142 offset:8192
	ds_read_b128 v[208:211], v142 offset:9216
	ds_read_b128 v[212:215], v142 offset:10240
	ds_read_b128 v[216:219], v142 offset:11264
	global_load_lds_dwordx4 v[220:221], off
	v_lshl_add_u64 v[192:193], v[192:193], 0, s[8:9]
	s_add_i32 m0, s29, 0xf000
	s_nop 0
	global_load_lds_dwordx4 v[192:193], off
	s_waitcnt vmcnt(8)
	s_waitcnt lgkmcnt(0)
	s_barrier
	s_setprio 1
	s_waitcnt lgkmcnt(0)
	v_mfma_f32_16x16x32_bf16 v[126:129], v[144:147], v[176:179], v[126:129]
	v_mfma_f32_16x16x32_bf16 v[122:125], v[152:155], v[176:179], v[122:125]
	v_mfma_f32_16x16x32_bf16 v[110:113], v[144:147], v[196:199], v[110:113]
	v_mfma_f32_16x16x32_bf16 v[106:109], v[152:155], v[196:199], v[106:109]
	v_mfma_f32_16x16x32_bf16 v[94:97], v[144:147], v[204:207], v[94:97]
	v_mfma_f32_16x16x32_bf16 v[90:93], v[152:155], v[204:207], v[90:93]
	v_mfma_f32_16x16x32_bf16 v[78:81], v[144:147], v[212:215], v[78:81]
	v_mfma_f32_16x16x32_bf16 v[74:77], v[152:155], v[212:215], v[74:77]
	v_mfma_f32_16x16x32_bf16 v[126:129], v[148:151], v[180:183], v[126:129]
	v_mfma_f32_16x16x32_bf16 v[122:125], v[156:159], v[180:183], v[122:125]
	v_mfma_f32_16x16x32_bf16 v[110:113], v[148:151], v[200:203], v[110:113]
	v_mfma_f32_16x16x32_bf16 v[106:109], v[156:159], v[200:203], v[106:109]
	v_mfma_f32_16x16x32_bf16 v[94:97], v[148:151], v[208:211], v[94:97]
	v_mfma_f32_16x16x32_bf16 v[90:93], v[156:159], v[208:211], v[90:93]
	v_mfma_f32_16x16x32_bf16 v[78:81], v[148:151], v[216:219], v[78:81]
	v_mfma_f32_16x16x32_bf16 v[74:77], v[156:159], v[216:219], v[74:77]
	s_setprio 0
	s_setprio 1
	v_mfma_f32_16x16x32_bf16 v[118:121], v[160:163], v[176:179], v[118:121]
	v_mfma_f32_16x16x32_bf16 v[114:117], v[168:171], v[176:179], v[114:117]
	v_mfma_f32_16x16x32_bf16 v[102:105], v[160:163], v[196:199], v[102:105]
	v_mfma_f32_16x16x32_bf16 v[98:101], v[168:171], v[196:199], v[98:101]
	v_mfma_f32_16x16x32_bf16 v[86:89], v[160:163], v[204:207], v[86:89]
	v_mfma_f32_16x16x32_bf16 v[82:85], v[168:171], v[204:207], v[82:85]
	v_mfma_f32_16x16x32_bf16 v[70:73], v[160:163], v[212:215], v[70:73]
	v_mfma_f32_16x16x32_bf16 v[66:69], v[168:171], v[212:215], v[66:69]
	v_mfma_f32_16x16x32_bf16 v[118:121], v[164:167], v[180:183], v[118:121]
	v_mfma_f32_16x16x32_bf16 v[114:117], v[172:175], v[180:183], v[114:117]
	v_mfma_f32_16x16x32_bf16 v[102:105], v[164:167], v[200:203], v[102:105]
	v_mfma_f32_16x16x32_bf16 v[98:101], v[172:175], v[200:203], v[98:101]
	v_mfma_f32_16x16x32_bf16 v[86:89], v[164:167], v[208:211], v[86:89]
	v_mfma_f32_16x16x32_bf16 v[82:85], v[172:175], v[208:211], v[82:85]
	v_mfma_f32_16x16x32_bf16 v[70:73], v[164:167], v[216:219], v[70:73]
	v_mfma_f32_16x16x32_bf16 v[66:69], v[172:175], v[216:219], v[66:69]
	s_setprio 0
	s_barrier
	s_add_i32 s45, s45, s2
	v_lshl_add_u64 v[192:193], s[74:75], 0, v[186:187]
	s_mov_b32 m0, s45
	ds_read_b128 v[176:179], v142 offset:20480
	ds_read_b128 v[180:183], v142 offset:21504
	ds_read_b128 v[196:199], v142 offset:22528
	ds_read_b128 v[200:203], v142 offset:23552
	ds_read_b128 v[204:207], v142 offset:24576
	ds_read_b128 v[208:211], v142 offset:25600
	ds_read_b128 v[212:215], v142 offset:26624
	ds_read_b128 v[216:219], v142 offset:27648
	global_load_lds_dwordx4 v186, s[74:75]
	v_lshl_add_u64 v[220:221], v[192:193], 0, s[82:83]
	s_add_i32 m0, s45, 0x2000
	s_add_i32 s45, s73, s2
	global_load_lds_dwordx4 v[220:221], off
	v_lshl_add_u64 v[220:221], v[192:193], 0, s[64:65]
	s_mov_b32 m0, s45
	v_lshl_add_u64 v[184:185], s[14:15], 0, v[184:185]
	global_load_lds_dwordx4 v[220:221], off
	v_lshl_add_u64 v[220:221], v[192:193], 0, s[86:87]
	s_add_i32 m0, s45, 0x2000
	s_nop 0
	global_load_lds_dwordx4 v[220:221], off
	s_mov_b32 m0, s33
	v_lshl_add_u64 v[220:221], v[184:185], 0, s[82:83]
	global_load_lds_dwordx4 v[184:185], off
	s_mov_b32 m0, s34
	s_nop 0
	global_load_lds_dwordx4 v[220:221], off
	s_waitcnt vmcnt(8)
	s_waitcnt lgkmcnt(0)
	s_barrier
	s_setprio 1
	s_waitcnt lgkmcnt(0)
	v_mfma_f32_16x16x32_bf16 v[62:65], v[144:147], v[176:179], v[62:65]
	v_mfma_f32_16x16x32_bf16 v[58:61], v[152:155], v[176:179], v[58:61]
	v_mfma_f32_16x16x32_bf16 v[46:49], v[144:147], v[196:199], v[46:49]
	v_mfma_f32_16x16x32_bf16 v[42:45], v[152:155], v[196:199], v[42:45]
	v_mfma_f32_16x16x32_bf16 v[30:33], v[144:147], v[204:207], v[30:33]
	v_mfma_f32_16x16x32_bf16 v[26:29], v[152:155], v[204:207], v[26:29]
	v_mfma_f32_16x16x32_bf16 v[14:17], v[144:147], v[212:215], v[14:17]
	v_mfma_f32_16x16x32_bf16 v[10:13], v[152:155], v[212:215], v[10:13]
	v_mfma_f32_16x16x32_bf16 v[62:65], v[148:151], v[180:183], v[62:65]
	v_mfma_f32_16x16x32_bf16 v[58:61], v[156:159], v[180:183], v[58:61]
	v_mfma_f32_16x16x32_bf16 v[46:49], v[148:151], v[200:203], v[46:49]
	v_mfma_f32_16x16x32_bf16 v[42:45], v[156:159], v[200:203], v[42:45]
	v_mfma_f32_16x16x32_bf16 v[30:33], v[148:151], v[208:211], v[30:33]
	v_mfma_f32_16x16x32_bf16 v[26:29], v[156:159], v[208:211], v[26:29]
	v_mfma_f32_16x16x32_bf16 v[14:17], v[148:151], v[216:219], v[14:17]
	v_mfma_f32_16x16x32_bf16 v[10:13], v[156:159], v[216:219], v[10:13]
	s_setprio 0
	s_setprio 1
	v_mfma_f32_16x16x32_bf16 v[54:57], v[160:163], v[176:179], v[54:57]
	v_mfma_f32_16x16x32_bf16 v[50:53], v[168:171], v[176:179], v[50:53]
	v_mfma_f32_16x16x32_bf16 v[38:41], v[160:163], v[196:199], v[38:41]
	v_mfma_f32_16x16x32_bf16 v[34:37], v[168:171], v[196:199], v[34:37]
	v_mfma_f32_16x16x32_bf16 v[22:25], v[160:163], v[204:207], v[22:25]
	v_mfma_f32_16x16x32_bf16 v[18:21], v[168:171], v[204:207], v[18:21]
	v_mfma_f32_16x16x32_bf16 v[6:9], v[160:163], v[212:215], v[6:9]
	v_mfma_f32_16x16x32_bf16 v[2:5], v[168:171], v[212:215], v[2:5]
	v_mfma_f32_16x16x32_bf16 v[54:57], v[164:167], v[180:183], v[54:57]
	v_mfma_f32_16x16x32_bf16 v[50:53], v[172:175], v[180:183], v[50:53]
	v_mfma_f32_16x16x32_bf16 v[38:41], v[164:167], v[200:203], v[38:41]
	v_mfma_f32_16x16x32_bf16 v[34:37], v[172:175], v[200:203], v[34:37]
	v_mfma_f32_16x16x32_bf16 v[22:25], v[164:167], v[208:211], v[22:25]
	v_mfma_f32_16x16x32_bf16 v[18:21], v[172:175], v[208:211], v[18:21]
	v_mfma_f32_16x16x32_bf16 v[6:9], v[164:167], v[216:219], v[6:9]
	v_mfma_f32_16x16x32_bf16 v[2:5], v[172:175], v[216:219], v[2:5]
	s_setprio 0
	s_barrier
	s_add_i32 s14, 0, 0x19000
	v_add_u32_e32 v131, s14, v1
	s_add_i32 s15, 0, 0x1d000
	ds_read_b128 v[144:147], v131
	ds_read_b128 v[148:151], v131 offset:1024
	ds_read_b128 v[152:155], v131 offset:2048
	ds_read_b128 v[156:159], v131 offset:3072
	v_add_u32_e32 v131, s15, v1
	ds_read_b128 v[160:163], v131
	ds_read_b128 v[164:167], v131 offset:1024
	ds_read_b128 v[168:171], v131 offset:2048
	ds_read_b128 v[172:175], v131 offset:3072
	s_mov_b32 m0, s35
	v_lshl_add_u64 v[220:221], v[184:185], 0, s[64:65]
	ds_read_b128 v[176:179], v142 offset:36864
	ds_read_b128 v[180:183], v142 offset:37888
	ds_read_b128 v[196:199], v142 offset:38912
	ds_read_b128 v[200:203], v142 offset:39936
	ds_read_b128 v[204:207], v142 offset:40960
	ds_read_b128 v[208:211], v142 offset:41984
	ds_read_b128 v[212:215], v142 offset:43008
	ds_read_b128 v[216:219], v142 offset:44032
	global_load_lds_dwordx4 v[220:221], off
	v_lshl_add_u64 v[220:221], v[184:185], 0, s[86:87]
	s_mov_b32 m0, s56
	s_nop 0
	global_load_lds_dwordx4 v[220:221], off
	s_waitcnt vmcnt(8)
	s_waitcnt lgkmcnt(0)
	s_barrier
	s_setprio 1
	s_waitcnt lgkmcnt(0)
	v_mfma_f32_16x16x32_bf16 v[126:129], v[144:147], v[176:179], v[126:129]
	v_mfma_f32_16x16x32_bf16 v[122:125], v[152:155], v[176:179], v[122:125]
	v_mfma_f32_16x16x32_bf16 v[110:113], v[144:147], v[196:199], v[110:113]
	v_mfma_f32_16x16x32_bf16 v[106:109], v[152:155], v[196:199], v[106:109]
	v_mfma_f32_16x16x32_bf16 v[94:97], v[144:147], v[204:207], v[94:97]
	v_mfma_f32_16x16x32_bf16 v[90:93], v[152:155], v[204:207], v[90:93]
	v_mfma_f32_16x16x32_bf16 v[78:81], v[144:147], v[212:215], v[78:81]
	v_mfma_f32_16x16x32_bf16 v[74:77], v[152:155], v[212:215], v[74:77]
	v_mfma_f32_16x16x32_bf16 v[126:129], v[148:151], v[180:183], v[126:129]
	v_mfma_f32_16x16x32_bf16 v[122:125], v[156:159], v[180:183], v[122:125]
	v_mfma_f32_16x16x32_bf16 v[110:113], v[148:151], v[200:203], v[110:113]
	v_mfma_f32_16x16x32_bf16 v[106:109], v[156:159], v[200:203], v[106:109]
	v_mfma_f32_16x16x32_bf16 v[94:97], v[148:151], v[208:211], v[94:97]
	v_mfma_f32_16x16x32_bf16 v[90:93], v[156:159], v[208:211], v[90:93]
	v_mfma_f32_16x16x32_bf16 v[78:81], v[148:151], v[216:219], v[78:81]
	v_mfma_f32_16x16x32_bf16 v[74:77], v[156:159], v[216:219], v[74:77]
	s_setprio 0
	s_setprio 1
	v_mfma_f32_16x16x32_bf16 v[118:121], v[160:163], v[176:179], v[118:121]
	v_mfma_f32_16x16x32_bf16 v[114:117], v[168:171], v[176:179], v[114:117]
	v_mfma_f32_16x16x32_bf16 v[102:105], v[160:163], v[196:199], v[102:105]
	v_mfma_f32_16x16x32_bf16 v[98:101], v[168:171], v[196:199], v[98:101]
	v_mfma_f32_16x16x32_bf16 v[86:89], v[160:163], v[204:207], v[86:89]
	v_mfma_f32_16x16x32_bf16 v[82:85], v[168:171], v[204:207], v[82:85]
	v_mfma_f32_16x16x32_bf16 v[70:73], v[160:163], v[212:215], v[70:73]
	v_mfma_f32_16x16x32_bf16 v[66:69], v[168:171], v[212:215], v[66:69]
	v_mfma_f32_16x16x32_bf16 v[118:121], v[164:167], v[180:183], v[118:121]
	v_mfma_f32_16x16x32_bf16 v[114:117], v[172:175], v[180:183], v[114:117]
	v_mfma_f32_16x16x32_bf16 v[102:105], v[164:167], v[200:203], v[102:105]
	v_mfma_f32_16x16x32_bf16 v[98:101], v[172:175], v[200:203], v[98:101]
	v_mfma_f32_16x16x32_bf16 v[86:89], v[164:167], v[208:211], v[86:89]
	v_mfma_f32_16x16x32_bf16 v[82:85], v[172:175], v[208:211], v[82:85]
	v_mfma_f32_16x16x32_bf16 v[70:73], v[164:167], v[216:219], v[70:73]
	v_mfma_f32_16x16x32_bf16 v[66:69], v[172:175], v[216:219], v[66:69]
	s_setprio 0
	s_barrier
	s_add_i32 s14, s14, s2
	v_lshl_add_u64 v[220:221], v[192:193], 0, s[92:93]
	s_mov_b32 m0, s14
	ds_read_b128 v[176:179], v142 offset:53248
	ds_read_b128 v[180:183], v142 offset:54272
	ds_read_b128 v[196:199], v142 offset:55296
	ds_read_b128 v[200:203], v142 offset:56320
	ds_read_b128 v[204:207], v142 offset:57344
	ds_read_b128 v[208:211], v142 offset:58368
	ds_read_b128 v[212:215], v142 offset:59392
	ds_read_b128 v[216:219], v142 offset:60416
	global_load_lds_dwordx4 v[220:221], off
	v_lshl_add_u64 v[220:221], v[192:193], 0, s[4:5]
	s_add_i32 m0, s14, 0x2000
	s_add_i32 s14, s15, s2
	global_load_lds_dwordx4 v[220:221], off
	v_lshl_add_u64 v[220:221], v[192:193], 0, s[6:7]
	s_mov_b32 m0, s14
	v_lshl_add_u64 v[192:193], v[192:193], 0, s[8:9]
	global_load_lds_dwordx4 v[220:221], off
	s_add_i32 m0, s14, 0x2000
	s_nop 0
	global_load_lds_dwordx4 v[192:193], off
	v_lshl_add_u64 v[192:193], v[184:185], 0, s[92:93]
	s_mov_b32 m0, s59
	v_lshl_add_u64 v[184:185], v[184:185], 0, s[4:5]
	global_load_lds_dwordx4 v[192:193], off
	s_mov_b32 m0, s60
	s_nop 0
	global_load_lds_dwordx4 v[184:185], off
	s_waitcnt vmcnt(8)
	s_waitcnt lgkmcnt(0)
	s_barrier
	s_setprio 1
	s_waitcnt lgkmcnt(0)
	v_mfma_f32_16x16x32_bf16 v[62:65], v[144:147], v[176:179], v[62:65]
	v_mfma_f32_16x16x32_bf16 v[58:61], v[152:155], v[176:179], v[58:61]
	s_add_i32 s43, s43, 2
	v_mfma_f32_16x16x32_bf16 v[46:49], v[144:147], v[196:199], v[46:49]
	s_add_u32 s54, s54, 0x100
	v_mfma_f32_16x16x32_bf16 v[42:45], v[152:155], v[196:199], v[42:45]
	s_addc_u32 s55, s55, 0
	v_mfma_f32_16x16x32_bf16 v[30:33], v[144:147], v[204:207], v[30:33]
	s_add_u32 s14, s52, s54
	v_mfma_f32_16x16x32_bf16 v[26:29], v[152:155], v[204:207], v[26:29]
	s_addc_u32 s15, s53, s55
	v_mfma_f32_16x16x32_bf16 v[14:17], v[144:147], v[212:215], v[14:17]
	s_add_u32 s45, s14, 0x100
	v_mfma_f32_16x16x32_bf16 v[10:13], v[152:155], v[212:215], v[10:13]
	s_addc_u32 s73, s15, 0
	v_mfma_f32_16x16x32_bf16 v[62:65], v[148:151], v[180:183], v[62:65]
	s_add_u32 s74, s24, s54
	v_mfma_f32_16x16x32_bf16 v[58:61], v[156:159], v[180:183], v[58:61]
	s_addc_u32 s75, s25, s55
	v_mfma_f32_16x16x32_bf16 v[46:49], v[148:151], v[200:203], v[46:49]
	s_cmpk_eq_i32 s54, 0x700
	v_mfma_f32_16x16x32_bf16 v[42:45], v[156:159], v[200:203], v[42:45]
	s_cselect_b64 vcc, -1, 0
	v_mfma_f32_16x16x32_bf16 v[30:33], v[148:151], v[208:211], v[30:33]
	s_and_b64 s[14:15], vcc, exec
	v_mfma_f32_16x16x32_bf16 v[26:29], v[156:159], v[208:211], v[26:29]
	s_cselect_b32 s15, s47, s73
	v_mfma_f32_16x16x32_bf16 v[14:17], v[148:151], v[216:219], v[14:17]
	s_cselect_b32 s14, s46, s45
	v_mfma_f32_16x16x32_bf16 v[10:13], v[156:159], v[216:219], v[10:13]
	s_cselect_b32 s75, s49, s75
	s_setprio 0
	s_setprio 1
	v_mfma_f32_16x16x32_bf16 v[54:57], v[160:163], v[176:179], v[54:57]
	s_cselect_b32 s74, s48, s74
	v_mfma_f32_16x16x32_bf16 v[50:53], v[168:171], v[176:179], v[50:53]
	s_add_i32 s45, 0, 0x11000
	v_mfma_f32_16x16x32_bf16 v[38:41], v[160:163], v[196:199], v[38:41]
	s_add_i32 s73, 0, 0x15000
	v_mfma_f32_16x16x32_bf16 v[34:37], v[168:171], v[196:199], v[34:37]
	v_mfma_f32_16x16x32_bf16 v[22:25], v[160:163], v[204:207], v[22:25]
	v_mfma_f32_16x16x32_bf16 v[18:21], v[168:171], v[204:207], v[18:21]
	v_mfma_f32_16x16x32_bf16 v[6:9], v[160:163], v[212:215], v[6:9]
	v_mfma_f32_16x16x32_bf16 v[2:5], v[168:171], v[212:215], v[2:5]
	v_mfma_f32_16x16x32_bf16 v[54:57], v[164:167], v[180:183], v[54:57]
	v_mfma_f32_16x16x32_bf16 v[50:53], v[172:175], v[180:183], v[50:53]
	v_mfma_f32_16x16x32_bf16 v[38:41], v[164:167], v[200:203], v[38:41]
	v_mfma_f32_16x16x32_bf16 v[34:37], v[172:175], v[200:203], v[34:37]
	v_mfma_f32_16x16x32_bf16 v[22:25], v[164:167], v[208:211], v[22:25]
	v_mfma_f32_16x16x32_bf16 v[18:21], v[172:175], v[208:211], v[18:21]
	v_mfma_f32_16x16x32_bf16 v[6:9], v[164:167], v[216:219], v[6:9]
	v_mfma_f32_16x16x32_bf16 v[2:5], v[172:175], v[216:219], v[2:5]
	s_setprio 0
	s_barrier
	s_cmp_gt_u32 s43, 13
	s_cbranch_scc0 .LBB0_1111
	s_and_b64 vcc, exec, s[40:41]
	s_cbranch_vccz .LBB0_1114
	s_barrier

.Lup_tokskip:
	s_setprio 1
	s_waitcnt lgkmcnt(0)
	v_mfma_f32_16x16x32_bf16 v[70:73], v[78:81], v[204:207], 0
	v_mfma_f32_16x16x32_bf16 v[54:57], v[158:161], v[204:207], 0
	v_mfma_f32_16x16x32_bf16 v[46:49], v[78:81], v[212:215], 0
	v_mfma_f32_16x16x32_bf16 v[38:41], v[158:161], v[212:215], 0
	v_mfma_f32_16x16x32_bf16 v[30:33], v[78:81], v[220:223], 0
	v_mfma_f32_16x16x32_bf16 v[22:25], v[158:161], v[220:223], 0
	v_mfma_f32_16x16x32_bf16 v[14:17], v[78:81], v[244:247], 0
	v_mfma_f32_16x16x32_bf16 v[6:9], v[158:161], v[244:247], 0
	v_mfma_f32_16x16x32_bf16 v[70:73], v[154:157], v[208:211], v[70:73]
	v_mfma_f32_16x16x32_bf16 v[54:57], v[172:175], v[208:211], v[54:57]
	v_mfma_f32_16x16x32_bf16 v[46:49], v[154:157], v[216:219], v[46:49]
	v_mfma_f32_16x16x32_bf16 v[38:41], v[172:175], v[216:219], v[38:41]
	v_mfma_f32_16x16x32_bf16 v[30:33], v[154:157], v[240:243], v[30:33]
	v_mfma_f32_16x16x32_bf16 v[22:25], v[172:175], v[240:243], v[22:25]
	v_mfma_f32_16x16x32_bf16 v[14:17], v[154:157], v[248:251], v[14:17]
	v_mfma_f32_16x16x32_bf16 v[6:9], v[172:175], v[248:251], v[6:9]
	s_setprio 0
	s_setprio 1
	v_mfma_f32_16x16x32_bf16 v[66:69], v[176:179], v[204:207], 0
	v_mfma_f32_16x16x32_bf16 v[50:53], v[196:199], v[204:207], 0
	v_mfma_f32_16x16x32_bf16 v[42:45], v[176:179], v[212:215], 0
	v_mfma_f32_16x16x32_bf16 v[34:37], v[196:199], v[212:215], 0
	v_mfma_f32_16x16x32_bf16 v[26:29], v[176:179], v[220:223], 0
	v_mfma_f32_16x16x32_bf16 v[18:21], v[196:199], v[220:223], 0
	v_mfma_f32_16x16x32_bf16 v[10:13], v[176:179], v[244:247], 0
	v_mfma_f32_16x16x32_bf16 v[2:5], v[196:199], v[244:247], 0
	v_mfma_f32_16x16x32_bf16 v[66:69], v[180:183], v[208:211], v[66:69]
	v_mfma_f32_16x16x32_bf16 v[50:53], v[200:203], v[208:211], v[50:53]
	v_mfma_f32_16x16x32_bf16 v[42:45], v[180:183], v[216:219], v[42:45]
	v_mfma_f32_16x16x32_bf16 v[34:37], v[200:203], v[216:219], v[34:37]
	v_mfma_f32_16x16x32_bf16 v[26:29], v[180:183], v[240:243], v[26:29]
	v_mfma_f32_16x16x32_bf16 v[18:21], v[200:203], v[240:243], v[18:21]
	v_mfma_f32_16x16x32_bf16 v[10:13], v[180:183], v[248:251], v[10:13]
	v_mfma_f32_16x16x32_bf16 v[2:5], v[200:203], v[248:251], v[2:5]
	s_setprio 0
	s_barrier
	s_add_i32 s35, 0, 0x19000
	v_add_u32_e32 v63, s35, v165
	s_add_i32 s55, 0, 0x1d000
	ds_read_b128 v[78:81], v63
	ds_read_b128 v[154:157], v63 offset:1024
	ds_read_b128 v[158:161], v63 offset:2048
	ds_read_b128 v[172:175], v63 offset:3072
	v_add_u32_e32 v63, s55, v165
	ds_read_b128 v[176:179], v63
	ds_read_b128 v[180:183], v63 offset:1024
	ds_read_b128 v[196:199], v63 offset:2048
	ds_read_b128 v[200:203], v63 offset:3072
	s_mov_b32 m0, s29
	ds_read_b128 v[204:207], v166 offset:36864
	ds_read_b128 v[208:211], v166 offset:37888
	ds_read_b128 v[212:215], v166 offset:38912
	ds_read_b128 v[216:219], v166 offset:39936
	ds_read_b128 v[220:223], v166 offset:40960
	ds_read_b128 v[240:243], v166 offset:41984
	ds_read_b128 v[244:247], v166 offset:43008
	ds_read_b128 v[248:251], v166 offset:44032
	global_load_lds_dwordx4 v59, s[14:15]
	s_mov_b32 m0, s33
	s_nop 0
	global_load_lds_dwordx4 v61, s[14:15]
	s_waitcnt vmcnt(8)
	s_waitcnt lgkmcnt(0)
	s_barrier
	s_setprio 1
	s_waitcnt lgkmcnt(0)
	v_mfma_f32_16x16x32_bf16 v[142:145], v[78:81], v[204:207], v[142:145]
	v_mfma_f32_16x16x32_bf16 v[134:137], v[158:161], v[204:207], v[134:137]
	v_mfma_f32_16x16x32_bf16 v[126:129], v[78:81], v[212:215], v[126:129]
	v_mfma_f32_16x16x32_bf16 v[118:121], v[158:161], v[212:215], v[118:121]
	v_mfma_f32_16x16x32_bf16 v[110:113], v[78:81], v[220:223], v[110:113]
	v_mfma_f32_16x16x32_bf16 v[102:105], v[158:161], v[220:223], v[102:105]
	v_mfma_f32_16x16x32_bf16 v[94:97], v[78:81], v[244:247], v[94:97]
	v_mfma_f32_16x16x32_bf16 v[86:89], v[158:161], v[244:247], v[86:89]
	v_mfma_f32_16x16x32_bf16 v[142:145], v[154:157], v[208:211], v[142:145]
	v_mfma_f32_16x16x32_bf16 v[134:137], v[172:175], v[208:211], v[134:137]
	v_mfma_f32_16x16x32_bf16 v[126:129], v[154:157], v[216:219], v[126:129]
	v_mfma_f32_16x16x32_bf16 v[118:121], v[172:175], v[216:219], v[118:121]
	v_mfma_f32_16x16x32_bf16 v[110:113], v[154:157], v[240:243], v[110:113]
	v_mfma_f32_16x16x32_bf16 v[102:105], v[172:175], v[240:243], v[102:105]
	v_mfma_f32_16x16x32_bf16 v[94:97], v[154:157], v[248:251], v[94:97]
	v_mfma_f32_16x16x32_bf16 v[86:89], v[172:175], v[248:251], v[86:89]
	s_setprio 0
	s_setprio 1
	v_mfma_f32_16x16x32_bf16 v[138:141], v[176:179], v[204:207], v[138:141]
	v_mfma_f32_16x16x32_bf16 v[130:133], v[196:199], v[204:207], v[130:133]
	v_mfma_f32_16x16x32_bf16 v[122:125], v[176:179], v[212:215], v[122:125]
	v_mfma_f32_16x16x32_bf16 v[114:117], v[196:199], v[212:215], v[114:117]
	v_mfma_f32_16x16x32_bf16 v[106:109], v[176:179], v[220:223], v[106:109]
	v_mfma_f32_16x16x32_bf16 v[98:101], v[196:199], v[220:223], v[98:101]
	v_mfma_f32_16x16x32_bf16 v[90:93], v[176:179], v[244:247], v[90:93]
	v_mfma_f32_16x16x32_bf16 v[82:85], v[196:199], v[244:247], v[82:85]
	v_mfma_f32_16x16x32_bf16 v[138:141], v[180:183], v[208:211], v[138:141]
	v_mfma_f32_16x16x32_bf16 v[130:133], v[200:203], v[208:211], v[130:133]
	v_mfma_f32_16x16x32_bf16 v[122:125], v[180:183], v[216:219], v[122:125]
	v_mfma_f32_16x16x32_bf16 v[114:117], v[200:203], v[216:219], v[114:117]
	v_mfma_f32_16x16x32_bf16 v[106:109], v[180:183], v[240:243], v[106:109]
	v_mfma_f32_16x16x32_bf16 v[98:101], v[200:203], v[240:243], v[98:101]
	v_mfma_f32_16x16x32_bf16 v[90:93], v[180:183], v[248:251], v[90:93]
	v_mfma_f32_16x16x32_bf16 v[82:85], v[200:203], v[248:251], v[82:85]
	s_setprio 0
	s_barrier
	s_add_i32 s14, s35, s17
	v_lshl_add_u64 v[230:231], v[192:193], 0, s[92:93]
	s_mov_b32 m0, s14
	ds_read_b128 v[204:207], v166 offset:53248
	ds_read_b128 v[208:211], v166 offset:54272
	ds_read_b128 v[212:215], v166 offset:55296
	ds_read_b128 v[216:219], v166 offset:56320
	ds_read_b128 v[220:223], v166 offset:57344
	ds_read_b128 v[240:243], v166 offset:58368
	ds_read_b128 v[244:247], v166 offset:59392
	ds_read_b128 v[248:251], v166 offset:60416
	global_load_lds_dwordx4 v[230:231], off
	v_lshl_add_u64 v[230:231], v[192:193], 0, s[4:5]
	s_add_i32 m0, s14, 0x2000
	s_add_i32 s14, s55, s17
	global_load_lds_dwordx4 v[230:231], off
	v_lshl_add_u64 v[230:231], v[192:193], 0, s[6:7]
	s_mov_b32 m0, s14
	v_lshl_add_u64 v[192:193], v[192:193], 0, s[8:9]
	global_load_lds_dwordx4 v[230:231], off
	s_add_i32 m0, s14, 0x2000
	v_lshl_add_u64 v[184:185], v[184:185], 0, s[92:93]
	global_load_lds_dwordx4 v[192:193], off
	v_lshl_add_u64 v[192:193], v[224:225], 0, s[92:93]
	s_mov_b32 m0, s80
	s_nop 0
	global_load_lds_dwordx4 v[192:193], off
	s_mov_b32 m0, s81
	s_nop 0
	global_load_lds_dwordx4 v[184:185], off
	s_waitcnt vmcnt(8)
	s_waitcnt lgkmcnt(0)
	s_barrier
	s_setprio 1
	s_waitcnt lgkmcnt(0)
	v_mfma_f32_16x16x32_bf16 v[70:73], v[78:81], v[204:207], v[70:73]
	v_mfma_f32_16x16x32_bf16 v[54:57], v[158:161], v[204:207], v[54:57]
	s_add_i32 s34, s34, 2
	v_mfma_f32_16x16x32_bf16 v[46:49], v[78:81], v[212:215], v[46:49]
	s_add_u32 s40, s40, 0x100
	v_mfma_f32_16x16x32_bf16 v[38:41], v[158:161], v[212:215], v[38:41]
	s_addc_u32 s41, s41, 0
	v_mfma_f32_16x16x32_bf16 v[30:33], v[78:81], v[220:223], v[30:33]
	s_add_u32 s14, s70, s40
	v_mfma_f32_16x16x32_bf16 v[22:25], v[158:161], v[220:223], v[22:25]
	s_addc_u32 s15, s71, s41
	v_mfma_f32_16x16x32_bf16 v[14:17], v[78:81], v[244:247], v[14:17]
	s_add_u32 s35, s14, 0x100
	v_mfma_f32_16x16x32_bf16 v[6:9], v[158:161], v[244:247], v[6:9]
	s_addc_u32 s55, s15, 0
	v_mfma_f32_16x16x32_bf16 v[70:73], v[154:157], v[208:211], v[70:73]
	s_add_u32 s61, s1, s40
	v_mfma_f32_16x16x32_bf16 v[54:57], v[172:175], v[208:211], v[54:57]
	s_addc_u32 s69, s2, s41
	v_mfma_f32_16x16x32_bf16 v[46:49], v[154:157], v[216:219], v[46:49]
	s_cmpk_eq_i32 s40, 0x700
	v_mfma_f32_16x16x32_bf16 v[38:41], v[172:175], v[216:219], v[38:41]
	s_cselect_b64 vcc, -1, 0
	v_mfma_f32_16x16x32_bf16 v[30:33], v[154:157], v[240:243], v[30:33]
	s_and_b64 s[14:15], vcc, exec
	v_mfma_f32_16x16x32_bf16 v[22:25], v[172:175], v[240:243], v[22:25]
	s_cselect_b32 s15, s59, s55
	v_mfma_f32_16x16x32_bf16 v[14:17], v[154:157], v[248:251], v[14:17]
	s_cselect_b32 s14, s58, s35
	v_mfma_f32_16x16x32_bf16 v[6:9], v[172:175], v[248:251], v[6:9]
	s_cselect_b32 s73, s57, s69
	s_setprio 0
	s_setprio 1
	v_mfma_f32_16x16x32_bf16 v[66:69], v[176:179], v[204:207], v[66:69]
	s_cselect_b32 s72, s56, s61
	v_mfma_f32_16x16x32_bf16 v[50:53], v[196:199], v[204:207], v[50:53]
	s_add_i32 s35, 0, 0x11000
	v_mfma_f32_16x16x32_bf16 v[42:45], v[176:179], v[212:215], v[42:45]
	s_add_i32 s55, 0, 0x15000
	v_mfma_f32_16x16x32_bf16 v[34:37], v[196:199], v[212:215], v[34:37]
	v_mfma_f32_16x16x32_bf16 v[26:29], v[176:179], v[220:223], v[26:29]
	v_mfma_f32_16x16x32_bf16 v[18:21], v[196:199], v[220:223], v[18:21]
	v_mfma_f32_16x16x32_bf16 v[10:13], v[176:179], v[244:247], v[10:13]
	v_mfma_f32_16x16x32_bf16 v[2:5], v[196:199], v[244:247], v[2:5]
	v_mfma_f32_16x16x32_bf16 v[66:69], v[180:183], v[208:211], v[66:69]
	v_mfma_f32_16x16x32_bf16 v[50:53], v[200:203], v[208:211], v[50:53]
	v_mfma_f32_16x16x32_bf16 v[42:45], v[180:183], v[216:219], v[42:45]
	v_mfma_f32_16x16x32_bf16 v[34:37], v[200:203], v[216:219], v[34:37]
	v_mfma_f32_16x16x32_bf16 v[26:29], v[180:183], v[240:243], v[26:29]
	v_mfma_f32_16x16x32_bf16 v[18:21], v[200:203], v[240:243], v[18:21]
	v_mfma_f32_16x16x32_bf16 v[10:13], v[180:183], v[248:251], v[10:13]
	v_mfma_f32_16x16x32_bf16 v[2:5], v[200:203], v[248:251], v[2:5]
	s_setprio 0
	s_barrier
.LBB0_1339:
	v_add_u32_e32 v63, s35, v165
	ds_read_b128 v[78:81], v63
	ds_read_b128 v[154:157], v63 offset:1024
	ds_read_b128 v[158:161], v63 offset:2048
	ds_read_b128 v[172:175], v63 offset:3072
	v_add_u32_e32 v63, s55, v165
	ds_read_b128 v[176:179], v63
	ds_read_b128 v[180:183], v63 offset:1024
	ds_read_b128 v[196:199], v63 offset:2048
	ds_read_b128 v[200:203], v63 offset:3072
	v_cndmask_b32_e32 v186, v62, v171, vcc
	v_cndmask_b32_e32 v184, v60, v170, vcc
	v_cndmask_b32_e32 v59, v58, v168, vcc
	v_cndmask_b32_e32 v61, v64, v169, vcc
	v_lshl_add_u64 v[192:193], v[76:77], 0, s[40:41]
	s_add_i32 m0, s24, 0xd000
	ds_read_b128 v[204:207], v166 offset:4096
	ds_read_b128 v[208:211], v166 offset:5120
	ds_read_b128 v[212:215], v166 offset:6144
	ds_read_b128 v[216:219], v166 offset:7168
	ds_read_b128 v[220:223], v166 offset:8192
	ds_read_b128 v[240:243], v166 offset:9216
	ds_read_b128 v[244:247], v166 offset:10240
	ds_read_b128 v[248:251], v166 offset:11264
	global_load_lds_dwordx4 v[192:193], off
	v_lshl_add_u64 v[192:193], v[74:75], 0, s[40:41]
	s_add_i32 m0, s24, 0xf000
	s_nop 0
	global_load_lds_dwordx4 v[192:193], off
	s_waitcnt vmcnt(8)
	s_waitcnt lgkmcnt(0)
	s_barrier
	s_setprio 1
	s_waitcnt lgkmcnt(0)
	v_mfma_f32_16x16x32_bf16 v[142:145], v[78:81], v[204:207], v[142:145]
	v_mfma_f32_16x16x32_bf16 v[134:137], v[158:161], v[204:207], v[134:137]
	v_mfma_f32_16x16x32_bf16 v[126:129], v[78:81], v[212:215], v[126:129]
	v_mfma_f32_16x16x32_bf16 v[118:121], v[158:161], v[212:215], v[118:121]
	v_mfma_f32_16x16x32_bf16 v[110:113], v[78:81], v[220:223], v[110:113]
	v_mfma_f32_16x16x32_bf16 v[102:105], v[158:161], v[220:223], v[102:105]
	v_mfma_f32_16x16x32_bf16 v[94:97], v[78:81], v[244:247], v[94:97]
	v_mfma_f32_16x16x32_bf16 v[86:89], v[158:161], v[244:247], v[86:89]
	v_mfma_f32_16x16x32_bf16 v[142:145], v[154:157], v[208:211], v[142:145]
	v_mfma_f32_16x16x32_bf16 v[134:137], v[172:175], v[208:211], v[134:137]
	v_mfma_f32_16x16x32_bf16 v[126:129], v[154:157], v[216:219], v[126:129]
	v_mfma_f32_16x16x32_bf16 v[118:121], v[172:175], v[216:219], v[118:121]
	v_mfma_f32_16x16x32_bf16 v[110:113], v[154:157], v[240:243], v[110:113]
	v_mfma_f32_16x16x32_bf16 v[102:105], v[172:175], v[240:243], v[102:105]
	v_mfma_f32_16x16x32_bf16 v[94:97], v[154:157], v[248:251], v[94:97]
	v_mfma_f32_16x16x32_bf16 v[86:89], v[172:175], v[248:251], v[86:89]
	s_setprio 0
	s_setprio 1
	v_mfma_f32_16x16x32_bf16 v[138:141], v[176:179], v[204:207], v[138:141]
	v_mfma_f32_16x16x32_bf16 v[130:133], v[196:199], v[204:207], v[130:133]
	v_mfma_f32_16x16x32_bf16 v[122:125], v[176:179], v[212:215], v[122:125]
	v_mfma_f32_16x16x32_bf16 v[114:117], v[196:199], v[212:215], v[114:117]
	v_mfma_f32_16x16x32_bf16 v[106:109], v[176:179], v[220:223], v[106:109]
	v_mfma_f32_16x16x32_bf16 v[98:101], v[196:199], v[220:223], v[98:101]
	v_mfma_f32_16x16x32_bf16 v[90:93], v[176:179], v[244:247], v[90:93]
	v_mfma_f32_16x16x32_bf16 v[82:85], v[196:199], v[244:247], v[82:85]
	v_mfma_f32_16x16x32_bf16 v[138:141], v[180:183], v[208:211], v[138:141]
	v_mfma_f32_16x16x32_bf16 v[130:133], v[200:203], v[208:211], v[130:133]
	v_mfma_f32_16x16x32_bf16 v[122:125], v[180:183], v[216:219], v[122:125]
	v_mfma_f32_16x16x32_bf16 v[114:117], v[200:203], v[216:219], v[114:117]
	v_mfma_f32_16x16x32_bf16 v[106:109], v[180:183], v[240:243], v[106:109]
	v_mfma_f32_16x16x32_bf16 v[98:101], v[200:203], v[240:243], v[98:101]
	v_mfma_f32_16x16x32_bf16 v[90:93], v[180:183], v[248:251], v[90:93]
	v_mfma_f32_16x16x32_bf16 v[82:85], v[200:203], v[248:251], v[82:85]
	s_setprio 0
	s_barrier
	s_add_i32 s35, s35, s17
	v_lshl_add_u64 v[192:193], s[72:73], 0, v[148:149]
	s_mov_b32 m0, s35
	ds_read_b128 v[204:207], v166 offset:20480
	ds_read_b128 v[208:211], v166 offset:21504
	ds_read_b128 v[212:215], v166 offset:22528
	ds_read_b128 v[216:219], v166 offset:23552
	ds_read_b128 v[220:223], v166 offset:24576
	ds_read_b128 v[240:243], v166 offset:25600
	ds_read_b128 v[244:247], v166 offset:26624
	ds_read_b128 v[248:251], v166 offset:27648
	global_load_lds_dwordx4 v[192:193], off
	v_lshl_add_u64 v[224:225], v[192:193], 0, s[82:83]
	s_add_i32 m0, s35, 0x2000
	s_add_i32 s35, s55, s17
	global_load_lds_dwordx4 v[224:225], off
	v_lshl_add_u64 v[224:225], v[192:193], 0, s[64:65]
	s_mov_b32 m0, s35
	v_mov_b32_e32 v185, v187
	global_load_lds_dwordx4 v[224:225], off
	v_lshl_add_u64 v[224:225], v[192:193], 0, s[86:87]
	s_add_i32 m0, s35, 0x2000
	s_nop 0
	global_load_lds_dwordx4 v[224:225], off
	s_mov_b32 m0, s25
	v_lshl_add_u64 v[224:225], s[14:15], 0, v[186:187]
	global_load_lds_dwordx4 v186, s[14:15]
	s_mov_b32 m0, s28
	s_nop 0
	global_load_lds_dwordx4 v184, s[14:15]
	s_waitcnt vmcnt(8)
	s_waitcnt lgkmcnt(0)
	v_lshl_add_u64 v[184:185], s[14:15], 0, v[184:185]
	s_barrier
	s_setprio 1
	s_waitcnt lgkmcnt(0)
	v_mfma_f32_16x16x32_bf16 v[70:73], v[78:81], v[204:207], v[70:73]
	v_mfma_f32_16x16x32_bf16 v[54:57], v[158:161], v[204:207], v[54:57]
	v_mfma_f32_16x16x32_bf16 v[46:49], v[78:81], v[212:215], v[46:49]
	v_mfma_f32_16x16x32_bf16 v[38:41], v[158:161], v[212:215], v[38:41]
	v_mfma_f32_16x16x32_bf16 v[30:33], v[78:81], v[220:223], v[30:33]
	v_mfma_f32_16x16x32_bf16 v[22:25], v[158:161], v[220:223], v[22:25]
	v_mfma_f32_16x16x32_bf16 v[14:17], v[78:81], v[244:247], v[14:17]
	v_mfma_f32_16x16x32_bf16 v[6:9], v[158:161], v[244:247], v[6:9]
	v_mfma_f32_16x16x32_bf16 v[70:73], v[154:157], v[208:211], v[70:73]
	v_mfma_f32_16x16x32_bf16 v[54:57], v[172:175], v[208:211], v[54:57]
	v_mfma_f32_16x16x32_bf16 v[46:49], v[154:157], v[216:219], v[46:49]
	v_mfma_f32_16x16x32_bf16 v[38:41], v[172:175], v[216:219], v[38:41]
	v_mfma_f32_16x16x32_bf16 v[30:33], v[154:157], v[240:243], v[30:33]
	v_mfma_f32_16x16x32_bf16 v[22:25], v[172:175], v[240:243], v[22:25]
	v_mfma_f32_16x16x32_bf16 v[14:17], v[154:157], v[248:251], v[14:17]
	v_mfma_f32_16x16x32_bf16 v[6:9], v[172:175], v[248:251], v[6:9]
	s_setprio 0
	s_setprio 1
	v_mfma_f32_16x16x32_bf16 v[66:69], v[176:179], v[204:207], v[66:69]
	v_mfma_f32_16x16x32_bf16 v[50:53], v[196:199], v[204:207], v[50:53]
	v_mfma_f32_16x16x32_bf16 v[42:45], v[176:179], v[212:215], v[42:45]
	v_mfma_f32_16x16x32_bf16 v[34:37], v[196:199], v[212:215], v[34:37]
	v_mfma_f32_16x16x32_bf16 v[26:29], v[176:179], v[220:223], v[26:29]
	v_mfma_f32_16x16x32_bf16 v[18:21], v[196:199], v[220:223], v[18:21]
	v_mfma_f32_16x16x32_bf16 v[10:13], v[176:179], v[244:247], v[10:13]
	v_mfma_f32_16x16x32_bf16 v[2:5], v[196:199], v[244:247], v[2:5]
	v_mfma_f32_16x16x32_bf16 v[66:69], v[180:183], v[208:211], v[66:69]
	v_mfma_f32_16x16x32_bf16 v[50:53], v[200:203], v[208:211], v[50:53]
	v_mfma_f32_16x16x32_bf16 v[42:45], v[180:183], v[216:219], v[42:45]
	v_mfma_f32_16x16x32_bf16 v[34:37], v[200:203], v[216:219], v[34:37]
	v_mfma_f32_16x16x32_bf16 v[26:29], v[180:183], v[240:243], v[26:29]
	v_mfma_f32_16x16x32_bf16 v[18:21], v[200:203], v[240:243], v[18:21]
	v_mfma_f32_16x16x32_bf16 v[10:13], v[180:183], v[248:251], v[10:13]
	v_mfma_f32_16x16x32_bf16 v[2:5], v[200:203], v[248:251], v[2:5]
	s_setprio 0
	s_barrier
	s_add_i32 s35, 0, 0x19000
	v_add_u32_e32 v63, s35, v165
	s_add_i32 s55, 0, 0x1d000
	ds_read_b128 v[78:81], v63
	ds_read_b128 v[154:157], v63 offset:1024
	ds_read_b128 v[158:161], v63 offset:2048
	ds_read_b128 v[172:175], v63 offset:3072
	v_add_u32_e32 v63, s55, v165
	ds_read_b128 v[176:179], v63
	ds_read_b128 v[180:183], v63 offset:1024
	ds_read_b128 v[196:199], v63 offset:2048
	ds_read_b128 v[200:203], v63 offset:3072
	s_mov_b32 m0, s29
	ds_read_b128 v[204:207], v166 offset:36864
	ds_read_b128 v[208:211], v166 offset:37888
	ds_read_b128 v[212:215], v166 offset:38912
	ds_read_b128 v[216:219], v166 offset:39936
	ds_read_b128 v[220:223], v166 offset:40960
	ds_read_b128 v[240:243], v166 offset:41984
	ds_read_b128 v[244:247], v166 offset:43008
	ds_read_b128 v[248:251], v166 offset:44032
	global_load_lds_dwordx4 v59, s[14:15]
	s_mov_b32 m0, s33
	s_nop 0
	global_load_lds_dwordx4 v61, s[14:15]
	s_waitcnt vmcnt(8)
	s_waitcnt lgkmcnt(0)
	s_barrier
	s_setprio 1
	s_waitcnt lgkmcnt(0)
	v_mfma_f32_16x16x32_bf16 v[142:145], v[78:81], v[204:207], v[142:145]
	v_mfma_f32_16x16x32_bf16 v[134:137], v[158:161], v[204:207], v[134:137]
	v_mfma_f32_16x16x32_bf16 v[126:129], v[78:81], v[212:215], v[126:129]
	v_mfma_f32_16x16x32_bf16 v[118:121], v[158:161], v[212:215], v[118:121]
	v_mfma_f32_16x16x32_bf16 v[110:113], v[78:81], v[220:223], v[110:113]
	v_mfma_f32_16x16x32_bf16 v[102:105], v[158:161], v[220:223], v[102:105]
	v_mfma_f32_16x16x32_bf16 v[94:97], v[78:81], v[244:247], v[94:97]
	v_mfma_f32_16x16x32_bf16 v[86:89], v[158:161], v[244:247], v[86:89]
	v_mfma_f32_16x16x32_bf16 v[142:145], v[154:157], v[208:211], v[142:145]
	v_mfma_f32_16x16x32_bf16 v[134:137], v[172:175], v[208:211], v[134:137]
	v_mfma_f32_16x16x32_bf16 v[126:129], v[154:157], v[216:219], v[126:129]
	v_mfma_f32_16x16x32_bf16 v[118:121], v[172:175], v[216:219], v[118:121]
	v_mfma_f32_16x16x32_bf16 v[110:113], v[154:157], v[240:243], v[110:113]
	v_mfma_f32_16x16x32_bf16 v[102:105], v[172:175], v[240:243], v[102:105]
	v_mfma_f32_16x16x32_bf16 v[94:97], v[154:157], v[248:251], v[94:97]
	v_mfma_f32_16x16x32_bf16 v[86:89], v[172:175], v[248:251], v[86:89]
	s_setprio 0
	s_setprio 1
	v_mfma_f32_16x16x32_bf16 v[138:141], v[176:179], v[204:207], v[138:141]
	v_mfma_f32_16x16x32_bf16 v[130:133], v[196:199], v[204:207], v[130:133]
	v_mfma_f32_16x16x32_bf16 v[122:125], v[176:179], v[212:215], v[122:125]
	v_mfma_f32_16x16x32_bf16 v[114:117], v[196:199], v[212:215], v[114:117]
	v_mfma_f32_16x16x32_bf16 v[106:109], v[176:179], v[220:223], v[106:109]
	v_mfma_f32_16x16x32_bf16 v[98:101], v[196:199], v[220:223], v[98:101]
	v_mfma_f32_16x16x32_bf16 v[90:93], v[176:179], v[244:247], v[90:93]
	v_mfma_f32_16x16x32_bf16 v[82:85], v[196:199], v[244:247], v[82:85]
	v_mfma_f32_16x16x32_bf16 v[138:141], v[180:183], v[208:211], v[138:141]
	v_mfma_f32_16x16x32_bf16 v[130:133], v[200:203], v[208:211], v[130:133]
	v_mfma_f32_16x16x32_bf16 v[122:125], v[180:183], v[216:219], v[122:125]
	v_mfma_f32_16x16x32_bf16 v[114:117], v[200:203], v[216:219], v[114:117]
	v_mfma_f32_16x16x32_bf16 v[106:109], v[180:183], v[240:243], v[106:109]
	v_mfma_f32_16x16x32_bf16 v[98:101], v[200:203], v[240:243], v[98:101]
	v_mfma_f32_16x16x32_bf16 v[90:93], v[180:183], v[248:251], v[90:93]
	v_mfma_f32_16x16x32_bf16 v[82:85], v[200:203], v[248:251], v[82:85]
	s_setprio 0
	s_barrier
	s_add_i32 s14, s35, s17
	v_lshl_add_u64 v[230:231], v[192:193], 0, s[92:93]
	s_mov_b32 m0, s14
	ds_read_b128 v[204:207], v166 offset:53248
	ds_read_b128 v[208:211], v166 offset:54272
	ds_read_b128 v[212:215], v166 offset:55296
	ds_read_b128 v[216:219], v166 offset:56320
	ds_read_b128 v[220:223], v166 offset:57344
	ds_read_b128 v[240:243], v166 offset:58368
	ds_read_b128 v[244:247], v166 offset:59392
	ds_read_b128 v[248:251], v166 offset:60416
	global_load_lds_dwordx4 v[230:231], off
	v_lshl_add_u64 v[230:231], v[192:193], 0, s[4:5]
	s_add_i32 m0, s14, 0x2000
	s_add_i32 s14, s55, s17
	global_load_lds_dwordx4 v[230:231], off
	v_lshl_add_u64 v[230:231], v[192:193], 0, s[6:7]
	s_mov_b32 m0, s14
	v_lshl_add_u64 v[192:193], v[192:193], 0, s[8:9]
	global_load_lds_dwordx4 v[230:231], off
	s_add_i32 m0, s14, 0x2000
	v_lshl_add_u64 v[184:185], v[184:185], 0, s[92:93]
	global_load_lds_dwordx4 v[192:193], off
	v_lshl_add_u64 v[192:193], v[224:225], 0, s[92:93]
	s_mov_b32 m0, s80
	s_nop 0
	global_load_lds_dwordx4 v[192:193], off
	s_mov_b32 m0, s81
	s_nop 0
	global_load_lds_dwordx4 v[184:185], off
	s_waitcnt vmcnt(8)
	s_waitcnt lgkmcnt(0)
	s_barrier
	s_setprio 1
	s_waitcnt lgkmcnt(0)
	v_mfma_f32_16x16x32_bf16 v[70:73], v[78:81], v[204:207], v[70:73]
	v_mfma_f32_16x16x32_bf16 v[54:57], v[158:161], v[204:207], v[54:57]
	s_add_i32 s34, s34, 2
	v_mfma_f32_16x16x32_bf16 v[46:49], v[78:81], v[212:215], v[46:49]
	s_add_u32 s40, s40, 0x100
	v_mfma_f32_16x16x32_bf16 v[38:41], v[158:161], v[212:215], v[38:41]
	s_addc_u32 s41, s41, 0
	v_mfma_f32_16x16x32_bf16 v[30:33], v[78:81], v[220:223], v[30:33]
	s_add_u32 s14, s70, s40
	v_mfma_f32_16x16x32_bf16 v[22:25], v[158:161], v[220:223], v[22:25]
	s_addc_u32 s15, s71, s41
	v_mfma_f32_16x16x32_bf16 v[14:17], v[78:81], v[244:247], v[14:17]
	s_add_u32 s35, s14, 0x100
	v_mfma_f32_16x16x32_bf16 v[6:9], v[158:161], v[244:247], v[6:9]
	s_addc_u32 s55, s15, 0
	v_mfma_f32_16x16x32_bf16 v[70:73], v[154:157], v[208:211], v[70:73]
	s_add_u32 s61, s1, s40
	v_mfma_f32_16x16x32_bf16 v[54:57], v[172:175], v[208:211], v[54:57]
	s_addc_u32 s69, s2, s41
	v_mfma_f32_16x16x32_bf16 v[46:49], v[154:157], v[216:219], v[46:49]
	s_cmpk_eq_i32 s40, 0x700
	v_mfma_f32_16x16x32_bf16 v[38:41], v[172:175], v[216:219], v[38:41]
	s_cselect_b64 vcc, -1, 0
	v_mfma_f32_16x16x32_bf16 v[30:33], v[154:157], v[240:243], v[30:33]
	s_and_b64 s[14:15], vcc, exec
	v_mfma_f32_16x16x32_bf16 v[22:25], v[172:175], v[240:243], v[22:25]
	s_cselect_b32 s15, s59, s55
	v_mfma_f32_16x16x32_bf16 v[14:17], v[154:157], v[248:251], v[14:17]
	s_cselect_b32 s14, s58, s35
	v_mfma_f32_16x16x32_bf16 v[6:9], v[172:175], v[248:251], v[6:9]
	s_cselect_b32 s73, s57, s69
	s_setprio 0
	s_setprio 1
	v_mfma_f32_16x16x32_bf16 v[66:69], v[176:179], v[204:207], v[66:69]
	s_cselect_b32 s72, s56, s61
	v_mfma_f32_16x16x32_bf16 v[50:53], v[196:199], v[204:207], v[50:53]
	s_add_i32 s35, 0, 0x11000
	v_mfma_f32_16x16x32_bf16 v[42:45], v[176:179], v[212:215], v[42:45]
	s_add_i32 s55, 0, 0x15000
	v_mfma_f32_16x16x32_bf16 v[34:37], v[196:199], v[212:215], v[34:37]
	v_mfma_f32_16x16x32_bf16 v[26:29], v[176:179], v[220:223], v[26:29]
	v_mfma_f32_16x16x32_bf16 v[18:21], v[196:199], v[220:223], v[18:21]
	v_mfma_f32_16x16x32_bf16 v[10:13], v[176:179], v[244:247], v[10:13]
	v_mfma_f32_16x16x32_bf16 v[2:5], v[196:199], v[244:247], v[2:5]
	v_mfma_f32_16x16x32_bf16 v[66:69], v[180:183], v[208:211], v[66:69]
	v_mfma_f32_16x16x32_bf16 v[50:53], v[200:203], v[208:211], v[50:53]
	v_mfma_f32_16x16x32_bf16 v[42:45], v[180:183], v[216:219], v[42:45]
	v_mfma_f32_16x16x32_bf16 v[34:37], v[200:203], v[216:219], v[34:37]
	v_mfma_f32_16x16x32_bf16 v[26:29], v[180:183], v[240:243], v[26:29]
	v_mfma_f32_16x16x32_bf16 v[18:21], v[200:203], v[240:243], v[18:21]
	v_mfma_f32_16x16x32_bf16 v[10:13], v[180:183], v[248:251], v[10:13]
	v_mfma_f32_16x16x32_bf16 v[2:5], v[200:203], v[248:251], v[2:5]
	s_setprio 0
	s_barrier
	s_cmp_gt_u32 s34, 13
	s_cbranch_scc0 .LBB0_1339
	s_lshl_b32 s1, s60, 8
	s_or_b32 s14, s1, s84
	s_ashr_i32 s15, s14, 31
	s_lshl_b64 s[14:15], s[14:15], 2
	s_add_u32 s1, s74, s14
	s_addc_u32 s2, s75, s15
	s_ashr_i32 s69, s68, 31
	s_lshl_b64 s[14:15], s[68:69], 13
	s_add_u32 s14, s1, s14
	s_addc_u32 s15, s2, s15
	v_lshl_add_u64 v[78:79], s[14:15], 0, v[150:151]
	global_load_dwordx4 v[58:61], v[78:79], off offset:48
	global_load_dwordx4 v[62:65], v[78:79], off offset:32
	global_load_dwordx4 v[74:77], v[78:79], off offset:16
	s_nop 0
	global_load_dwordx4 v[78:81], v[78:79], off
	s_and_b64 vcc, exec, s[50:51]
	s_cbranch_vccz .LBB0_1342
	s_barrier

.LBB0_1462:
	s_add_u32 s2, s56, 0x100
	s_addc_u32 s24, s57, 0
	s_add_u32 s56, s58, 0x40080
	s_waitcnt lgkmcnt(0)
	s_addc_u32 s57, s59, 0
	s_mov_b32 s25, -2
	s_add_u32 s14, s56, 0xfffc0080
	s_addc_u32 s15, s57, -1
	s_add_i32 s49, 0, 0x11000
	s_cmp_eq_u32 s25, 12
	s_cselect_b32 s15, s53, s15
	s_cselect_b32 s14, s52, s14
	v_add_u32_e32 v155, s49, v1
	s_cselect_b32 s35, s51, s24
	s_cselect_b32 s34, s50, s2
	s_add_i32 s55, 0, 0x15000
	ds_read_b128 v[156:159], v155
	ds_read_b128 v[160:163], v155 offset:1024
	ds_read_b128 v[164:167], v155 offset:2048
	ds_read_b128 v[168:171], v155 offset:3072
	v_add_u32_e32 v155, s55, v1
	ds_read_b128 v[172:175], v155
	ds_read_b128 v[176:179], v155 offset:1024
	ds_read_b128 v[180:183], v155 offset:2048
	ds_read_b128 v[196:199], v155 offset:3072
	v_lshl_add_u64 v[184:185], s[56:57], 0, v[152:153]
	s_add_i32 m0, s61, 0xd000
	ds_read_b128 v[200:203], v154 offset:4096
	ds_read_b128 v[204:207], v154 offset:5120
	ds_read_b128 v[208:211], v154 offset:6144
	ds_read_b128 v[212:215], v154 offset:7168
	ds_read_b128 v[216:219], v154 offset:8192
	ds_read_b128 v[220:223], v154 offset:9216
	ds_read_b128 v[240:243], v154 offset:10240
	ds_read_b128 v[244:247], v154 offset:11264
	global_load_lds_dwordx4 v[184:185], off
	v_lshl_add_u64 v[184:185], v[184:185], 0, s[82:83]
	s_add_i32 m0, s61, 0xf000
	s_nop 0
	global_load_lds_dwordx4 v[184:185], off
	s_waitcnt vmcnt(8)
	s_waitcnt lgkmcnt(0)
	s_barrier
	s_setprio 1
	s_waitcnt lgkmcnt(0)
	v_mfma_f32_16x16x32_bf16 v[142:145], v[156:159], v[200:203], 0
	v_mfma_f32_16x16x32_bf16 v[138:141], v[164:167], v[200:203], 0
	v_mfma_f32_16x16x32_bf16 v[126:129], v[156:159], v[208:211], 0
	v_mfma_f32_16x16x32_bf16 v[122:125], v[164:167], v[208:211], 0
	v_mfma_f32_16x16x32_bf16 v[110:113], v[156:159], v[216:219], 0
	v_mfma_f32_16x16x32_bf16 v[106:109], v[164:167], v[216:219], 0
	v_mfma_f32_16x16x32_bf16 v[94:97], v[156:159], v[240:243], 0
	v_mfma_f32_16x16x32_bf16 v[90:93], v[164:167], v[240:243], 0
	v_mfma_f32_16x16x32_bf16 v[142:145], v[160:163], v[204:207], v[142:145]
	v_mfma_f32_16x16x32_bf16 v[138:141], v[168:171], v[204:207], v[138:141]
	v_mfma_f32_16x16x32_bf16 v[126:129], v[160:163], v[212:215], v[126:129]
	v_mfma_f32_16x16x32_bf16 v[122:125], v[168:171], v[212:215], v[122:125]
	v_mfma_f32_16x16x32_bf16 v[110:113], v[160:163], v[220:223], v[110:113]
	v_mfma_f32_16x16x32_bf16 v[106:109], v[168:171], v[220:223], v[106:109]
	v_mfma_f32_16x16x32_bf16 v[94:97], v[160:163], v[244:247], v[94:97]
	v_mfma_f32_16x16x32_bf16 v[90:93], v[168:171], v[244:247], v[90:93]
	s_setprio 0
	s_setprio 1
	v_mfma_f32_16x16x32_bf16 v[134:137], v[172:175], v[200:203], 0
	v_mfma_f32_16x16x32_bf16 v[130:133], v[180:183], v[200:203], 0
	v_mfma_f32_16x16x32_bf16 v[118:121], v[172:175], v[208:211], 0
	v_mfma_f32_16x16x32_bf16 v[114:117], v[180:183], v[208:211], 0
	v_mfma_f32_16x16x32_bf16 v[102:105], v[172:175], v[216:219], 0
	v_mfma_f32_16x16x32_bf16 v[98:101], v[180:183], v[216:219], 0
	v_mfma_f32_16x16x32_bf16 v[86:89], v[172:175], v[240:243], 0
	v_mfma_f32_16x16x32_bf16 v[82:85], v[180:183], v[240:243], 0
	v_mfma_f32_16x16x32_bf16 v[134:137], v[176:179], v[204:207], v[134:137]
	v_mfma_f32_16x16x32_bf16 v[130:133], v[196:199], v[204:207], v[130:133]
	v_mfma_f32_16x16x32_bf16 v[118:121], v[176:179], v[212:215], v[118:121]
	v_mfma_f32_16x16x32_bf16 v[114:117], v[196:199], v[212:215], v[114:117]
	v_mfma_f32_16x16x32_bf16 v[102:105], v[176:179], v[220:223], v[102:105]
	v_mfma_f32_16x16x32_bf16 v[98:101], v[196:199], v[220:223], v[98:101]
	v_mfma_f32_16x16x32_bf16 v[86:89], v[176:179], v[244:247], v[86:89]
	v_mfma_f32_16x16x32_bf16 v[82:85], v[196:199], v[244:247], v[82:85]
	s_setprio 0
	s_barrier
	v_lshl_add_u64 v[184:185], s[34:35], 0, v[186:187]
	s_add_i32 s34, s49, s28
	s_mov_b32 m0, s34
	ds_read_b128 v[200:203], v154 offset:20480
	ds_read_b128 v[204:207], v154 offset:21504
	ds_read_b128 v[208:211], v154 offset:22528
	ds_read_b128 v[212:215], v154 offset:23552
	ds_read_b128 v[216:219], v154 offset:24576
	ds_read_b128 v[220:223], v154 offset:25600
	ds_read_b128 v[240:243], v154 offset:26624
	ds_read_b128 v[244:247], v154 offset:27648
	global_load_lds_dwordx4 v[184:185], off
	v_lshl_add_u64 v[192:193], v[184:185], 0, s[82:83]
	s_add_i32 m0, s34, 0x2000
	s_add_i32 s34, s55, s28
	global_load_lds_dwordx4 v[192:193], off
	v_lshl_add_u64 v[192:193], v[184:185], 0, s[64:65]
	s_mov_b32 m0, s34
	s_nop 0
	global_load_lds_dwordx4 v[192:193], off
	v_lshl_add_u64 v[192:193], v[184:185], 0, s[86:87]
	s_add_i32 m0, s34, 0x2000
	s_nop 0
	global_load_lds_dwordx4 v[192:193], off
	v_lshl_add_u64 v[192:193], s[14:15], 0, v[146:147]
	s_mov_b32 m0, s68
	v_lshl_add_u64 v[224:225], v[192:193], 0, s[82:83]
	global_load_lds_dwordx4 v[192:193], off
	s_mov_b32 m0, s69
	s_nop 0
	global_load_lds_dwordx4 v[224:225], off
	s_waitcnt vmcnt(8)
	s_waitcnt lgkmcnt(0)
	s_barrier
	s_setprio 1
	s_waitcnt lgkmcnt(0)
	v_mfma_f32_16x16x32_bf16 v[78:81], v[156:159], v[200:203], 0
	v_mfma_f32_16x16x32_bf16 v[74:77], v[164:167], v[200:203], 0
	v_mfma_f32_16x16x32_bf16 v[62:65], v[156:159], v[208:211], 0
	v_mfma_f32_16x16x32_bf16 v[58:61], v[164:167], v[208:211], 0
	v_mfma_f32_16x16x32_bf16 v[46:49], v[156:159], v[216:219], 0
	v_mfma_f32_16x16x32_bf16 v[42:45], v[164:167], v[216:219], 0
	v_mfma_f32_16x16x32_bf16 v[30:33], v[156:159], v[240:243], 0
	v_mfma_f32_16x16x32_bf16 v[26:29], v[164:167], v[240:243], 0
	v_mfma_f32_16x16x32_bf16 v[78:81], v[160:163], v[204:207], v[78:81]
	v_mfma_f32_16x16x32_bf16 v[74:77], v[168:171], v[204:207], v[74:77]
	v_mfma_f32_16x16x32_bf16 v[62:65], v[160:163], v[212:215], v[62:65]
	v_mfma_f32_16x16x32_bf16 v[58:61], v[168:171], v[212:215], v[58:61]
	v_mfma_f32_16x16x32_bf16 v[46:49], v[160:163], v[220:223], v[46:49]
	v_mfma_f32_16x16x32_bf16 v[42:45], v[168:171], v[220:223], v[42:45]
	v_mfma_f32_16x16x32_bf16 v[30:33], v[160:163], v[244:247], v[30:33]
	v_mfma_f32_16x16x32_bf16 v[26:29], v[168:171], v[244:247], v[26:29]
	s_setprio 0
	s_setprio 1
	v_mfma_f32_16x16x32_bf16 v[70:73], v[172:175], v[200:203], 0
	v_mfma_f32_16x16x32_bf16 v[66:69], v[180:183], v[200:203], 0
	v_mfma_f32_16x16x32_bf16 v[54:57], v[172:175], v[208:211], 0
	v_mfma_f32_16x16x32_bf16 v[50:53], v[180:183], v[208:211], 0
	v_mfma_f32_16x16x32_bf16 v[38:41], v[172:175], v[216:219], 0
	v_mfma_f32_16x16x32_bf16 v[34:37], v[180:183], v[216:219], 0
	v_mfma_f32_16x16x32_bf16 v[22:25], v[172:175], v[240:243], 0
	v_mfma_f32_16x16x32_bf16 v[18:21], v[180:183], v[240:243], 0
	v_mfma_f32_16x16x32_bf16 v[70:73], v[176:179], v[204:207], v[70:73]
	v_mfma_f32_16x16x32_bf16 v[66:69], v[196:199], v[204:207], v[66:69]
	v_mfma_f32_16x16x32_bf16 v[54:57], v[176:179], v[212:215], v[54:57]
	v_mfma_f32_16x16x32_bf16 v[50:53], v[196:199], v[212:215], v[50:53]
	v_mfma_f32_16x16x32_bf16 v[38:41], v[176:179], v[220:223], v[38:41]
	v_mfma_f32_16x16x32_bf16 v[34:37], v[196:199], v[220:223], v[34:37]
	v_mfma_f32_16x16x32_bf16 v[22:25], v[176:179], v[244:247], v[22:25]
	v_mfma_f32_16x16x32_bf16 v[18:21], v[196:199], v[244:247], v[18:21]
	s_setprio 0
	s_barrier
	s_add_i32 s14, 0, 0x19000
	v_add_u32_e32 v155, s14, v1
	s_add_i32 s15, 0, 0x1d000
	ds_read_b128 v[156:159], v155
	ds_read_b128 v[160:163], v155 offset:1024
	ds_read_b128 v[164:167], v155 offset:2048
	ds_read_b128 v[168:171], v155 offset:3072
	v_add_u32_e32 v155, s15, v1
	ds_read_b128 v[172:175], v155
	ds_read_b128 v[176:179], v155 offset:1024
	ds_read_b128 v[180:183], v155 offset:2048
	ds_read_b128 v[196:199], v155 offset:3072
	s_mov_b32 m0, s70
	v_lshl_add_u64 v[224:225], v[192:193], 0, s[64:65]
	ds_read_b128 v[200:203], v154 offset:36864
	ds_read_b128 v[204:207], v154 offset:37888
	ds_read_b128 v[208:211], v154 offset:38912
	ds_read_b128 v[212:215], v154 offset:39936
	ds_read_b128 v[216:219], v154 offset:40960
	ds_read_b128 v[220:223], v154 offset:41984
	ds_read_b128 v[240:243], v154 offset:43008
	ds_read_b128 v[244:247], v154 offset:44032
	global_load_lds_dwordx4 v[224:225], off
	v_lshl_add_u64 v[224:225], v[192:193], 0, s[86:87]
	s_mov_b32 m0, s71
	s_nop 0
	global_load_lds_dwordx4 v[224:225], off
	s_waitcnt vmcnt(8)
	s_waitcnt lgkmcnt(0)
	s_barrier
	s_setprio 1
	s_waitcnt lgkmcnt(0)
	v_mfma_f32_16x16x32_bf16 v[142:145], v[156:159], v[200:203], v[142:145]
	v_mfma_f32_16x16x32_bf16 v[138:141], v[164:167], v[200:203], v[138:141]
	v_mfma_f32_16x16x32_bf16 v[126:129], v[156:159], v[208:211], v[126:129]
	v_mfma_f32_16x16x32_bf16 v[122:125], v[164:167], v[208:211], v[122:125]
	v_mfma_f32_16x16x32_bf16 v[110:113], v[156:159], v[216:219], v[110:113]
	v_mfma_f32_16x16x32_bf16 v[106:109], v[164:167], v[216:219], v[106:109]
	v_mfma_f32_16x16x32_bf16 v[94:97], v[156:159], v[240:243], v[94:97]
	v_mfma_f32_16x16x32_bf16 v[90:93], v[164:167], v[240:243], v[90:93]
	v_mfma_f32_16x16x32_bf16 v[142:145], v[160:163], v[204:207], v[142:145]
	v_mfma_f32_16x16x32_bf16 v[138:141], v[168:171], v[204:207], v[138:141]
	v_mfma_f32_16x16x32_bf16 v[126:129], v[160:163], v[212:215], v[126:129]
	v_mfma_f32_16x16x32_bf16 v[122:125], v[168:171], v[212:215], v[122:125]
	v_mfma_f32_16x16x32_bf16 v[110:113], v[160:163], v[220:223], v[110:113]
	v_mfma_f32_16x16x32_bf16 v[106:109], v[168:171], v[220:223], v[106:109]
	v_mfma_f32_16x16x32_bf16 v[94:97], v[160:163], v[244:247], v[94:97]
	v_mfma_f32_16x16x32_bf16 v[90:93], v[168:171], v[244:247], v[90:93]
	s_setprio 0
	s_setprio 1
	v_mfma_f32_16x16x32_bf16 v[134:137], v[172:175], v[200:203], v[134:137]
	v_mfma_f32_16x16x32_bf16 v[130:133], v[180:183], v[200:203], v[130:133]
	v_mfma_f32_16x16x32_bf16 v[118:121], v[172:175], v[208:211], v[118:121]
	v_mfma_f32_16x16x32_bf16 v[114:117], v[180:183], v[208:211], v[114:117]
	v_mfma_f32_16x16x32_bf16 v[102:105], v[172:175], v[216:219], v[102:105]
	v_mfma_f32_16x16x32_bf16 v[98:101], v[180:183], v[216:219], v[98:101]
	v_mfma_f32_16x16x32_bf16 v[86:89], v[172:175], v[240:243], v[86:89]
	v_mfma_f32_16x16x32_bf16 v[82:85], v[180:183], v[240:243], v[82:85]
	v_mfma_f32_16x16x32_bf16 v[134:137], v[176:179], v[204:207], v[134:137]
	v_mfma_f32_16x16x32_bf16 v[130:133], v[196:199], v[204:207], v[130:133]
	v_mfma_f32_16x16x32_bf16 v[118:121], v[176:179], v[212:215], v[118:121]
	v_mfma_f32_16x16x32_bf16 v[114:117], v[196:199], v[212:215], v[114:117]
	v_mfma_f32_16x16x32_bf16 v[102:105], v[176:179], v[220:223], v[102:105]
	v_mfma_f32_16x16x32_bf16 v[98:101], v[196:199], v[220:223], v[98:101]
	v_mfma_f32_16x16x32_bf16 v[86:89], v[176:179], v[244:247], v[86:89]
	v_mfma_f32_16x16x32_bf16 v[82:85], v[196:199], v[244:247], v[82:85]
	s_setprio 0
	s_barrier
	s_add_i32 s14, s14, s28
	v_lshl_add_u64 v[224:225], v[184:185], 0, s[92:93]
	s_mov_b32 m0, s14
	ds_read_b128 v[200:203], v154 offset:53248
	ds_read_b128 v[204:207], v154 offset:54272
	ds_read_b128 v[208:211], v154 offset:55296
	ds_read_b128 v[212:215], v154 offset:56320
	ds_read_b128 v[216:219], v154 offset:57344
	ds_read_b128 v[220:223], v154 offset:58368
	ds_read_b128 v[240:243], v154 offset:59392
	ds_read_b128 v[244:247], v154 offset:60416
	global_load_lds_dwordx4 v[224:225], off
	v_lshl_add_u64 v[224:225], v[184:185], 0, s[4:5]
	s_add_i32 m0, s14, 0x2000
	s_add_i32 s14, s15, s28
	global_load_lds_dwordx4 v[224:225], off
	v_lshl_add_u64 v[224:225], v[184:185], 0, s[6:7]
	s_mov_b32 m0, s14
	v_lshl_add_u64 v[184:185], v[184:185], 0, s[8:9]
	global_load_lds_dwordx4 v[224:225], off
	s_add_i32 m0, s14, 0x2000
	s_nop 0
	global_load_lds_dwordx4 v[184:185], off
	v_lshl_add_u64 v[184:185], v[192:193], 0, s[92:93]
	s_mov_b32 m0, s75
	s_nop 0
	global_load_lds_dwordx4 v[184:185], off
	v_lshl_add_u64 v[184:185], v[192:193], 0, s[4:5]
	s_mov_b32 m0, s76
	s_nop 0
	global_load_lds_dwordx4 v[184:185], off
	s_waitcnt vmcnt(8)
	s_waitcnt lgkmcnt(0)
	s_barrier
	s_setprio 1
	s_waitcnt lgkmcnt(0)
	v_mfma_f32_16x16x32_bf16 v[78:81], v[156:159], v[200:203], v[78:81]
	v_mfma_f32_16x16x32_bf16 v[74:77], v[164:167], v[200:203], v[74:77]
	s_add_i32 s25, s25, 2
	v_mfma_f32_16x16x32_bf16 v[62:65], v[156:159], v[208:211], v[62:65]
	s_add_u32 s2, s2, 0x100
	v_mfma_f32_16x16x32_bf16 v[58:61], v[164:167], v[208:211], v[58:61]
	s_addc_u32 s24, s24, 0
	v_mfma_f32_16x16x32_bf16 v[46:49], v[156:159], v[216:219], v[46:49]
	s_add_u32 s56, s56, 0x100
	v_mfma_f32_16x16x32_bf16 v[42:45], v[164:167], v[216:219], v[42:45]
	s_addc_u32 s57, s57, 0
	v_mfma_f32_16x16x32_bf16 v[30:33], v[156:159], v[240:243], v[30:33]
	s_add_u32 s14, s56, 0xfffc0080
	v_mfma_f32_16x16x32_bf16 v[26:29], v[164:167], v[240:243], v[26:29]
	s_addc_u32 s15, s57, -1
	v_mfma_f32_16x16x32_bf16 v[78:81], v[160:163], v[204:207], v[78:81]
	s_add_i32 s49, 0, 0x11000
	v_mfma_f32_16x16x32_bf16 v[74:77], v[168:171], v[204:207], v[74:77]
	s_cmp_eq_u32 s25, 12
	v_mfma_f32_16x16x32_bf16 v[62:65], v[160:163], v[212:215], v[62:65]
	s_cselect_b32 s15, s53, s15
	v_mfma_f32_16x16x32_bf16 v[58:61], v[168:171], v[212:215], v[58:61]
	s_cselect_b32 s14, s52, s14
	v_mfma_f32_16x16x32_bf16 v[46:49], v[160:163], v[220:223], v[46:49]
	s_cselect_b32 s35, s51, s24
	v_mfma_f32_16x16x32_bf16 v[42:45], v[168:171], v[220:223], v[42:45]
	s_cselect_b32 s34, s50, s2
	v_mfma_f32_16x16x32_bf16 v[30:33], v[160:163], v[244:247], v[30:33]
	s_add_i32 s55, 0, 0x15000
	v_mfma_f32_16x16x32_bf16 v[26:29], v[168:171], v[244:247], v[26:29]
	s_setprio 0
	s_setprio 1
	v_mfma_f32_16x16x32_bf16 v[70:73], v[172:175], v[200:203], v[70:73]
	v_mfma_f32_16x16x32_bf16 v[66:69], v[180:183], v[200:203], v[66:69]
	v_mfma_f32_16x16x32_bf16 v[54:57], v[172:175], v[208:211], v[54:57]
	v_mfma_f32_16x16x32_bf16 v[50:53], v[180:183], v[208:211], v[50:53]
	v_mfma_f32_16x16x32_bf16 v[38:41], v[172:175], v[216:219], v[38:41]
	v_mfma_f32_16x16x32_bf16 v[34:37], v[180:183], v[216:219], v[34:37]
	v_mfma_f32_16x16x32_bf16 v[22:25], v[172:175], v[240:243], v[22:25]
	v_mfma_f32_16x16x32_bf16 v[18:21], v[180:183], v[240:243], v[18:21]
	v_mfma_f32_16x16x32_bf16 v[70:73], v[176:179], v[204:207], v[70:73]
	v_mfma_f32_16x16x32_bf16 v[66:69], v[196:199], v[204:207], v[66:69]
	v_mfma_f32_16x16x32_bf16 v[54:57], v[176:179], v[212:215], v[54:57]
	v_mfma_f32_16x16x32_bf16 v[50:53], v[196:199], v[212:215], v[50:53]
	v_mfma_f32_16x16x32_bf16 v[38:41], v[176:179], v[220:223], v[38:41]
	v_mfma_f32_16x16x32_bf16 v[34:37], v[196:199], v[220:223], v[34:37]
	v_mfma_f32_16x16x32_bf16 v[22:25], v[176:179], v[244:247], v[22:25]
	v_mfma_f32_16x16x32_bf16 v[18:21], v[196:199], v[244:247], v[18:21]
	s_setprio 0
	s_barrier
.LBB0_1463:
	v_add_u32_e32 v155, s49, v1
	ds_read_b128 v[156:159], v155
	ds_read_b128 v[160:163], v155 offset:1024
	ds_read_b128 v[164:167], v155 offset:2048
	ds_read_b128 v[168:171], v155 offset:3072
	v_add_u32_e32 v155, s55, v1
	ds_read_b128 v[172:175], v155
	ds_read_b128 v[176:179], v155 offset:1024
	ds_read_b128 v[180:183], v155 offset:2048
	ds_read_b128 v[196:199], v155 offset:3072
	v_lshl_add_u64 v[184:185], s[56:57], 0, v[152:153]
	s_add_i32 m0, s61, 0xd000
	ds_read_b128 v[200:203], v154 offset:4096
	ds_read_b128 v[204:207], v154 offset:5120
	ds_read_b128 v[208:211], v154 offset:6144
	ds_read_b128 v[212:215], v154 offset:7168
	ds_read_b128 v[216:219], v154 offset:8192
	ds_read_b128 v[220:223], v154 offset:9216
	ds_read_b128 v[240:243], v154 offset:10240
	ds_read_b128 v[244:247], v154 offset:11264
	global_load_lds_dwordx4 v[184:185], off
	v_lshl_add_u64 v[184:185], v[184:185], 0, s[82:83]
	s_add_i32 m0, s61, 0xf000
	s_nop 0
	global_load_lds_dwordx4 v[184:185], off
	s_waitcnt vmcnt(8)
	s_waitcnt lgkmcnt(0)
	s_barrier
	s_setprio 1
	s_waitcnt lgkmcnt(0)
	v_mfma_f32_16x16x32_bf16 v[142:145], v[156:159], v[200:203], v[142:145]
	v_mfma_f32_16x16x32_bf16 v[138:141], v[164:167], v[200:203], v[138:141]
	v_mfma_f32_16x16x32_bf16 v[126:129], v[156:159], v[208:211], v[126:129]
	v_mfma_f32_16x16x32_bf16 v[122:125], v[164:167], v[208:211], v[122:125]
	v_mfma_f32_16x16x32_bf16 v[110:113], v[156:159], v[216:219], v[110:113]
	v_mfma_f32_16x16x32_bf16 v[106:109], v[164:167], v[216:219], v[106:109]
	v_mfma_f32_16x16x32_bf16 v[94:97], v[156:159], v[240:243], v[94:97]
	v_mfma_f32_16x16x32_bf16 v[90:93], v[164:167], v[240:243], v[90:93]
	v_mfma_f32_16x16x32_bf16 v[142:145], v[160:163], v[204:207], v[142:145]
	v_mfma_f32_16x16x32_bf16 v[138:141], v[168:171], v[204:207], v[138:141]
	v_mfma_f32_16x16x32_bf16 v[126:129], v[160:163], v[212:215], v[126:129]
	v_mfma_f32_16x16x32_bf16 v[122:125], v[168:171], v[212:215], v[122:125]
	v_mfma_f32_16x16x32_bf16 v[110:113], v[160:163], v[220:223], v[110:113]
	v_mfma_f32_16x16x32_bf16 v[106:109], v[168:171], v[220:223], v[106:109]
	v_mfma_f32_16x16x32_bf16 v[94:97], v[160:163], v[244:247], v[94:97]
	v_mfma_f32_16x16x32_bf16 v[90:93], v[168:171], v[244:247], v[90:93]
	s_setprio 0
	s_setprio 1
	v_mfma_f32_16x16x32_bf16 v[134:137], v[172:175], v[200:203], v[134:137]
	v_mfma_f32_16x16x32_bf16 v[130:133], v[180:183], v[200:203], v[130:133]
	v_mfma_f32_16x16x32_bf16 v[118:121], v[172:175], v[208:211], v[118:121]
	v_mfma_f32_16x16x32_bf16 v[114:117], v[180:183], v[208:211], v[114:117]
	v_mfma_f32_16x16x32_bf16 v[102:105], v[172:175], v[216:219], v[102:105]
	v_mfma_f32_16x16x32_bf16 v[98:101], v[180:183], v[216:219], v[98:101]
	v_mfma_f32_16x16x32_bf16 v[86:89], v[172:175], v[240:243], v[86:89]
	v_mfma_f32_16x16x32_bf16 v[82:85], v[180:183], v[240:243], v[82:85]
	v_mfma_f32_16x16x32_bf16 v[134:137], v[176:179], v[204:207], v[134:137]
	v_mfma_f32_16x16x32_bf16 v[130:133], v[196:199], v[204:207], v[130:133]
	v_mfma_f32_16x16x32_bf16 v[118:121], v[176:179], v[212:215], v[118:121]
	v_mfma_f32_16x16x32_bf16 v[114:117], v[196:199], v[212:215], v[114:117]
	v_mfma_f32_16x16x32_bf16 v[102:105], v[176:179], v[220:223], v[102:105]
	v_mfma_f32_16x16x32_bf16 v[98:101], v[196:199], v[220:223], v[98:101]
	v_mfma_f32_16x16x32_bf16 v[86:89], v[176:179], v[244:247], v[86:89]
	v_mfma_f32_16x16x32_bf16 v[82:85], v[196:199], v[244:247], v[82:85]
	s_setprio 0
	s_barrier
	v_lshl_add_u64 v[184:185], s[34:35], 0, v[186:187]
	s_add_i32 s34, s49, s28
	s_mov_b32 m0, s34
	ds_read_b128 v[200:203], v154 offset:20480
	ds_read_b128 v[204:207], v154 offset:21504
	ds_read_b128 v[208:211], v154 offset:22528
	ds_read_b128 v[212:215], v154 offset:23552
	ds_read_b128 v[216:219], v154 offset:24576
	ds_read_b128 v[220:223], v154 offset:25600
	ds_read_b128 v[240:243], v154 offset:26624
	ds_read_b128 v[244:247], v154 offset:27648
	global_load_lds_dwordx4 v[184:185], off
	v_lshl_add_u64 v[192:193], v[184:185], 0, s[82:83]
	s_add_i32 m0, s34, 0x2000
	s_add_i32 s34, s55, s28
	global_load_lds_dwordx4 v[192:193], off
	v_lshl_add_u64 v[192:193], v[184:185], 0, s[64:65]
	s_mov_b32 m0, s34
	s_nop 0
	global_load_lds_dwordx4 v[192:193], off
	v_lshl_add_u64 v[192:193], v[184:185], 0, s[86:87]
	s_add_i32 m0, s34, 0x2000
	s_nop 0
	global_load_lds_dwordx4 v[192:193], off
	v_lshl_add_u64 v[192:193], s[14:15], 0, v[146:147]
	s_mov_b32 m0, s68
	v_lshl_add_u64 v[224:225], v[192:193], 0, s[82:83]
	global_load_lds_dwordx4 v[192:193], off
	s_mov_b32 m0, s69
	s_nop 0
	global_load_lds_dwordx4 v[224:225], off
	s_waitcnt vmcnt(8)
	s_waitcnt lgkmcnt(0)
	s_barrier
	s_setprio 1
	s_waitcnt lgkmcnt(0)
	v_mfma_f32_16x16x32_bf16 v[78:81], v[156:159], v[200:203], v[78:81]
	v_mfma_f32_16x16x32_bf16 v[74:77], v[164:167], v[200:203], v[74:77]
	v_mfma_f32_16x16x32_bf16 v[62:65], v[156:159], v[208:211], v[62:65]
	v_mfma_f32_16x16x32_bf16 v[58:61], v[164:167], v[208:211], v[58:61]
	v_mfma_f32_16x16x32_bf16 v[46:49], v[156:159], v[216:219], v[46:49]
	v_mfma_f32_16x16x32_bf16 v[42:45], v[164:167], v[216:219], v[42:45]
	v_mfma_f32_16x16x32_bf16 v[30:33], v[156:159], v[240:243], v[30:33]
	v_mfma_f32_16x16x32_bf16 v[26:29], v[164:167], v[240:243], v[26:29]
	v_mfma_f32_16x16x32_bf16 v[78:81], v[160:163], v[204:207], v[78:81]
	v_mfma_f32_16x16x32_bf16 v[74:77], v[168:171], v[204:207], v[74:77]
	v_mfma_f32_16x16x32_bf16 v[62:65], v[160:163], v[212:215], v[62:65]
	v_mfma_f32_16x16x32_bf16 v[58:61], v[168:171], v[212:215], v[58:61]
	v_mfma_f32_16x16x32_bf16 v[46:49], v[160:163], v[220:223], v[46:49]
	v_mfma_f32_16x16x32_bf16 v[42:45], v[168:171], v[220:223], v[42:45]
	v_mfma_f32_16x16x32_bf16 v[30:33], v[160:163], v[244:247], v[30:33]
	v_mfma_f32_16x16x32_bf16 v[26:29], v[168:171], v[244:247], v[26:29]
	s_setprio 0
	s_setprio 1
	v_mfma_f32_16x16x32_bf16 v[70:73], v[172:175], v[200:203], v[70:73]
	v_mfma_f32_16x16x32_bf16 v[66:69], v[180:183], v[200:203], v[66:69]
	v_mfma_f32_16x16x32_bf16 v[54:57], v[172:175], v[208:211], v[54:57]
	v_mfma_f32_16x16x32_bf16 v[50:53], v[180:183], v[208:211], v[50:53]
	v_mfma_f32_16x16x32_bf16 v[38:41], v[172:175], v[216:219], v[38:41]
	v_mfma_f32_16x16x32_bf16 v[34:37], v[180:183], v[216:219], v[34:37]
	v_mfma_f32_16x16x32_bf16 v[22:25], v[172:175], v[240:243], v[22:25]
	v_mfma_f32_16x16x32_bf16 v[18:21], v[180:183], v[240:243], v[18:21]
	v_mfma_f32_16x16x32_bf16 v[70:73], v[176:179], v[204:207], v[70:73]
	v_mfma_f32_16x16x32_bf16 v[66:69], v[196:199], v[204:207], v[66:69]
	v_mfma_f32_16x16x32_bf16 v[54:57], v[176:179], v[212:215], v[54:57]
	v_mfma_f32_16x16x32_bf16 v[50:53], v[196:199], v[212:215], v[50:53]
	v_mfma_f32_16x16x32_bf16 v[38:41], v[176:179], v[220:223], v[38:41]
	v_mfma_f32_16x16x32_bf16 v[34:37], v[196:199], v[220:223], v[34:37]
	v_mfma_f32_16x16x32_bf16 v[22:25], v[176:179], v[244:247], v[22:25]
	v_mfma_f32_16x16x32_bf16 v[18:21], v[196:199], v[244:247], v[18:21]
	s_setprio 0
	s_barrier
	s_add_i32 s14, 0, 0x19000
	v_add_u32_e32 v155, s14, v1
	s_add_i32 s15, 0, 0x1d000
	ds_read_b128 v[156:159], v155
	ds_read_b128 v[160:163], v155 offset:1024
	ds_read_b128 v[164:167], v155 offset:2048
	ds_read_b128 v[168:171], v155 offset:3072
	v_add_u32_e32 v155, s15, v1
	ds_read_b128 v[172:175], v155
	ds_read_b128 v[176:179], v155 offset:1024
	ds_read_b128 v[180:183], v155 offset:2048
	ds_read_b128 v[196:199], v155 offset:3072
	s_mov_b32 m0, s70
	v_lshl_add_u64 v[224:225], v[192:193], 0, s[64:65]
	ds_read_b128 v[200:203], v154 offset:36864
	ds_read_b128 v[204:207], v154 offset:37888
	ds_read_b128 v[208:211], v154 offset:38912
	ds_read_b128 v[212:215], v154 offset:39936
	ds_read_b128 v[216:219], v154 offset:40960
	ds_read_b128 v[220:223], v154 offset:41984
	ds_read_b128 v[240:243], v154 offset:43008
	ds_read_b128 v[244:247], v154 offset:44032
	global_load_lds_dwordx4 v[224:225], off
	v_lshl_add_u64 v[224:225], v[192:193], 0, s[86:87]
	s_mov_b32 m0, s71
	s_nop 0
	global_load_lds_dwordx4 v[224:225], off
	s_waitcnt vmcnt(8)
	s_waitcnt lgkmcnt(0)
	s_barrier
	s_setprio 1
	s_waitcnt lgkmcnt(0)
	v_mfma_f32_16x16x32_bf16 v[142:145], v[156:159], v[200:203], v[142:145]
	v_mfma_f32_16x16x32_bf16 v[138:141], v[164:167], v[200:203], v[138:141]
	v_mfma_f32_16x16x32_bf16 v[126:129], v[156:159], v[208:211], v[126:129]
	v_mfma_f32_16x16x32_bf16 v[122:125], v[164:167], v[208:211], v[122:125]
	v_mfma_f32_16x16x32_bf16 v[110:113], v[156:159], v[216:219], v[110:113]
	v_mfma_f32_16x16x32_bf16 v[106:109], v[164:167], v[216:219], v[106:109]
	v_mfma_f32_16x16x32_bf16 v[94:97], v[156:159], v[240:243], v[94:97]
	v_mfma_f32_16x16x32_bf16 v[90:93], v[164:167], v[240:243], v[90:93]
	v_mfma_f32_16x16x32_bf16 v[142:145], v[160:163], v[204:207], v[142:145]
	v_mfma_f32_16x16x32_bf16 v[138:141], v[168:171], v[204:207], v[138:141]
	v_mfma_f32_16x16x32_bf16 v[126:129], v[160:163], v[212:215], v[126:129]
	v_mfma_f32_16x16x32_bf16 v[122:125], v[168:171], v[212:215], v[122:125]
	v_mfma_f32_16x16x32_bf16 v[110:113], v[160:163], v[220:223], v[110:113]
	v_mfma_f32_16x16x32_bf16 v[106:109], v[168:171], v[220:223], v[106:109]
	v_mfma_f32_16x16x32_bf16 v[94:97], v[160:163], v[244:247], v[94:97]
	v_mfma_f32_16x16x32_bf16 v[90:93], v[168:171], v[244:247], v[90:93]
	s_setprio 0
	s_setprio 1
	v_mfma_f32_16x16x32_bf16 v[134:137], v[172:175], v[200:203], v[134:137]
	v_mfma_f32_16x16x32_bf16 v[130:133], v[180:183], v[200:203], v[130:133]
	v_mfma_f32_16x16x32_bf16 v[118:121], v[172:175], v[208:211], v[118:121]
	v_mfma_f32_16x16x32_bf16 v[114:117], v[180:183], v[208:211], v[114:117]
	v_mfma_f32_16x16x32_bf16 v[102:105], v[172:175], v[216:219], v[102:105]
	v_mfma_f32_16x16x32_bf16 v[98:101], v[180:183], v[216:219], v[98:101]
	v_mfma_f32_16x16x32_bf16 v[86:89], v[172:175], v[240:243], v[86:89]
	v_mfma_f32_16x16x32_bf16 v[82:85], v[180:183], v[240:243], v[82:85]
	v_mfma_f32_16x16x32_bf16 v[134:137], v[176:179], v[204:207], v[134:137]
	v_mfma_f32_16x16x32_bf16 v[130:133], v[196:199], v[204:207], v[130:133]
	v_mfma_f32_16x16x32_bf16 v[118:121], v[176:179], v[212:215], v[118:121]
	v_mfma_f32_16x16x32_bf16 v[114:117], v[196:199], v[212:215], v[114:117]
	v_mfma_f32_16x16x32_bf16 v[102:105], v[176:179], v[220:223], v[102:105]
	v_mfma_f32_16x16x32_bf16 v[98:101], v[196:199], v[220:223], v[98:101]
	v_mfma_f32_16x16x32_bf16 v[86:89], v[176:179], v[244:247], v[86:89]
	v_mfma_f32_16x16x32_bf16 v[82:85], v[196:199], v[244:247], v[82:85]
	s_setprio 0
	s_barrier
	s_add_i32 s14, s14, s28
	v_lshl_add_u64 v[224:225], v[184:185], 0, s[92:93]
	s_mov_b32 m0, s14
	ds_read_b128 v[200:203], v154 offset:53248
	ds_read_b128 v[204:207], v154 offset:54272
	ds_read_b128 v[208:211], v154 offset:55296
	ds_read_b128 v[212:215], v154 offset:56320
	ds_read_b128 v[216:219], v154 offset:57344
	ds_read_b128 v[220:223], v154 offset:58368
	ds_read_b128 v[240:243], v154 offset:59392
	ds_read_b128 v[244:247], v154 offset:60416
	global_load_lds_dwordx4 v[224:225], off
	v_lshl_add_u64 v[224:225], v[184:185], 0, s[4:5]
	s_add_i32 m0, s14, 0x2000
	s_add_i32 s14, s15, s28
	global_load_lds_dwordx4 v[224:225], off
	v_lshl_add_u64 v[224:225], v[184:185], 0, s[6:7]
	s_mov_b32 m0, s14
	v_lshl_add_u64 v[184:185], v[184:185], 0, s[8:9]
	global_load_lds_dwordx4 v[224:225], off
	s_add_i32 m0, s14, 0x2000
	s_nop 0
	global_load_lds_dwordx4 v[184:185], off
	v_lshl_add_u64 v[184:185], v[192:193], 0, s[92:93]
	s_mov_b32 m0, s75
	s_nop 0
	global_load_lds_dwordx4 v[184:185], off
	v_lshl_add_u64 v[184:185], v[192:193], 0, s[4:5]
	s_mov_b32 m0, s76
	s_nop 0
	global_load_lds_dwordx4 v[184:185], off
	s_waitcnt vmcnt(8)
	s_waitcnt lgkmcnt(0)
	s_barrier
	s_setprio 1
	s_waitcnt lgkmcnt(0)
	v_mfma_f32_16x16x32_bf16 v[78:81], v[156:159], v[200:203], v[78:81]
	v_mfma_f32_16x16x32_bf16 v[74:77], v[164:167], v[200:203], v[74:77]
	s_add_i32 s25, s25, 2
	v_mfma_f32_16x16x32_bf16 v[62:65], v[156:159], v[208:211], v[62:65]
	s_add_u32 s2, s2, 0x100
	v_mfma_f32_16x16x32_bf16 v[58:61], v[164:167], v[208:211], v[58:61]
	s_addc_u32 s24, s24, 0
	v_mfma_f32_16x16x32_bf16 v[46:49], v[156:159], v[216:219], v[46:49]
	s_add_u32 s56, s56, 0x100
	v_mfma_f32_16x16x32_bf16 v[42:45], v[164:167], v[216:219], v[42:45]
	s_addc_u32 s57, s57, 0
	v_mfma_f32_16x16x32_bf16 v[30:33], v[156:159], v[240:243], v[30:33]
	s_add_u32 s14, s56, 0xfffc0080
	v_mfma_f32_16x16x32_bf16 v[26:29], v[164:167], v[240:243], v[26:29]
	s_addc_u32 s15, s57, -1
	v_mfma_f32_16x16x32_bf16 v[78:81], v[160:163], v[204:207], v[78:81]
	s_add_i32 s49, 0, 0x11000
	v_mfma_f32_16x16x32_bf16 v[74:77], v[168:171], v[204:207], v[74:77]
	s_cmp_eq_u32 s25, 12
	v_mfma_f32_16x16x32_bf16 v[62:65], v[160:163], v[212:215], v[62:65]
	s_cselect_b32 s15, s53, s15
	v_mfma_f32_16x16x32_bf16 v[58:61], v[168:171], v[212:215], v[58:61]
	s_cselect_b32 s14, s52, s14
	v_mfma_f32_16x16x32_bf16 v[46:49], v[160:163], v[220:223], v[46:49]
	s_cselect_b32 s35, s51, s24
	v_mfma_f32_16x16x32_bf16 v[42:45], v[168:171], v[220:223], v[42:45]
	s_cselect_b32 s34, s50, s2
	v_mfma_f32_16x16x32_bf16 v[30:33], v[160:163], v[244:247], v[30:33]
	s_add_i32 s55, 0, 0x15000
	v_mfma_f32_16x16x32_bf16 v[26:29], v[168:171], v[244:247], v[26:29]
	s_setprio 0
	s_setprio 1
	v_mfma_f32_16x16x32_bf16 v[70:73], v[172:175], v[200:203], v[70:73]
	v_mfma_f32_16x16x32_bf16 v[66:69], v[180:183], v[200:203], v[66:69]
	v_mfma_f32_16x16x32_bf16 v[54:57], v[172:175], v[208:211], v[54:57]
	v_mfma_f32_16x16x32_bf16 v[50:53], v[180:183], v[208:211], v[50:53]
	v_mfma_f32_16x16x32_bf16 v[38:41], v[172:175], v[216:219], v[38:41]
	v_mfma_f32_16x16x32_bf16 v[34:37], v[180:183], v[216:219], v[34:37]
	v_mfma_f32_16x16x32_bf16 v[22:25], v[172:175], v[240:243], v[22:25]
	v_mfma_f32_16x16x32_bf16 v[18:21], v[180:183], v[240:243], v[18:21]
	v_mfma_f32_16x16x32_bf16 v[70:73], v[176:179], v[204:207], v[70:73]
	v_mfma_f32_16x16x32_bf16 v[66:69], v[196:199], v[204:207], v[66:69]
	v_mfma_f32_16x16x32_bf16 v[54:57], v[176:179], v[212:215], v[54:57]
	v_mfma_f32_16x16x32_bf16 v[50:53], v[196:199], v[212:215], v[50:53]
	v_mfma_f32_16x16x32_bf16 v[38:41], v[176:179], v[220:223], v[38:41]
	v_mfma_f32_16x16x32_bf16 v[34:37], v[196:199], v[220:223], v[34:37]
	v_mfma_f32_16x16x32_bf16 v[22:25], v[176:179], v[244:247], v[22:25]
	v_mfma_f32_16x16x32_bf16 v[18:21], v[196:199], v[244:247], v[18:21]
	s_setprio 0
	s_barrier
	s_cmp_gt_u32 s25, 13
	s_cbranch_scc0 .LBB0_1463
	s_and_b64 vcc, exec, s[46:47]
	s_cbranch_vccz .LBB0_1466
	s_barrier
